# dead-wait elimination: the lgkmcnt(7)/(6) waits at the head of bf16 8-read MMA segments (already covered by the pre-barrier lgkmcnt(6)) deleted
# baseline (speedup 1.0000x reference)
.LBB0_219:
	s_waitcnt lgkmcnt(0)
	s_add_i32 s4, s92, 0x180
	s_add_i32 s5, s93, 0x180
	s_barrier
	s_setprio 1
	s_waitcnt lgkmcnt(7)
	v_mfma_f32_16x16x32_bf16 v[60:63], v[156:159], v[188:191], 0
	s_waitcnt lgkmcnt(6)
	v_mfma_f32_16x16x32_bf16 v[60:63], v[152:155], v[184:187], v[60:63]
	v_mfma_f32_16x16x32_bf16 v[56:59], v[148:151], v[188:191], 0
	s_nop 0
	v_mfma_f32_16x16x32_bf16 v[56:59], v[144:147], v[184:187], v[56:59]
	s_waitcnt lgkmcnt(5)
	v_mfma_f32_16x16x32_bf16 v[52:55], v[156:159], v[180:183], 0
	s_waitcnt lgkmcnt(4)
	v_mfma_f32_16x16x32_bf16 v[52:55], v[152:155], v[176:179], v[52:55]
	v_mfma_f32_16x16x32_bf16 v[48:51], v[148:151], v[180:183], 0
	s_nop 0
	v_mfma_f32_16x16x32_bf16 v[48:51], v[144:147], v[176:179], v[48:51]
	s_waitcnt lgkmcnt(3)
	v_mfma_f32_16x16x32_bf16 v[44:47], v[156:159], v[172:175], 0
	s_waitcnt lgkmcnt(2)
	v_mfma_f32_16x16x32_bf16 v[44:47], v[152:155], v[168:171], v[44:47]
	v_mfma_f32_16x16x32_bf16 v[40:43], v[148:151], v[172:175], 0
	s_nop 0
	v_mfma_f32_16x16x32_bf16 v[40:43], v[144:147], v[168:171], v[40:43]
	s_waitcnt lgkmcnt(1)
	v_mfma_f32_16x16x32_bf16 v[36:39], v[156:159], v[164:167], 0
	s_waitcnt lgkmcnt(0)
	v_mfma_f32_16x16x32_bf16 v[36:39], v[152:155], v[160:163], v[36:39]
	v_mfma_f32_16x16x32_bf16 v[32:35], v[148:151], v[164:167], 0
	s_nop 0
	v_mfma_f32_16x16x32_bf16 v[32:35], v[144:147], v[160:163], v[32:35]
	s_setprio 0
	s_setprio 1
	v_mfma_f32_16x16x32_bf16 v[28:31], v[140:143], v[188:191], 0
	s_nop 0
	v_mfma_f32_16x16x32_bf16 v[28:31], v[136:139], v[184:187], v[28:31]
	v_mfma_f32_16x16x32_bf16 v[24:27], v[132:135], v[188:191], 0
	s_nop 0
	v_mfma_f32_16x16x32_bf16 v[24:27], v[128:131], v[184:187], v[24:27]
	v_mfma_f32_16x16x32_bf16 v[20:23], v[140:143], v[180:183], 0
	s_nop 0
	v_mfma_f32_16x16x32_bf16 v[20:23], v[136:139], v[176:179], v[20:23]
	v_mfma_f32_16x16x32_bf16 v[16:19], v[132:135], v[180:183], 0
	s_nop 0
	v_mfma_f32_16x16x32_bf16 v[16:19], v[128:131], v[176:179], v[16:19]
	v_mfma_f32_16x16x32_bf16 v[12:15], v[140:143], v[172:175], 0
	s_nop 0
	v_mfma_f32_16x16x32_bf16 v[12:15], v[136:139], v[168:171], v[12:15]
	v_mfma_f32_16x16x32_bf16 v[8:11], v[132:135], v[172:175], 0
	s_nop 0
	v_mfma_f32_16x16x32_bf16 v[8:11], v[128:131], v[168:171], v[8:11]
	v_mfma_f32_16x16x32_bf16 v[4:7], v[140:143], v[164:167], 0
	s_nop 0
	v_mfma_f32_16x16x32_bf16 v[4:7], v[136:139], v[160:163], v[4:7]
	v_mfma_f32_16x16x32_bf16 v[0:3], v[132:135], v[164:167], 0
	s_nop 0
	v_mfma_f32_16x16x32_bf16 v[0:3], v[128:131], v[160:163], v[0:3]
	s_setprio 0
	s_barrier
	ds_read_b128 v[156:159], v211
	ds_read_b128 v[152:155], v212
	ds_read_b128 v[148:151], v213
	ds_read_b128 v[144:147], v214
	ds_read_b128 v[140:143], v215
	ds_read_b128 v[136:139], v216
	ds_read_b128 v[132:135], v217
	ds_read_b128 v[128:131], v218
	ds_read_b128 v[160:163], v219 offset:32768
	ds_read_b128 v[164:167], v219 offset:33792
	ds_read_b128 v[168:171], v219 offset:34816
	ds_read_b128 v[172:175], v219 offset:35840
	ds_read_b128 v[176:179], v219 offset:36864
	ds_read_b128 v[180:183], v219 offset:37888
	ds_read_b128 v[184:187], v219 offset:38912
	ds_read_b128 v[188:191], v219 offset:39936
	s_mov_b32 m0, s69
	s_add_i32 s14, s92, 0x20100
	buffer_load_dwordx4 v196, s[8:11], s14 offen lds
	s_add_i32 s14, s92, 0x30100
	s_mov_b32 m0, s70
	s_nop 0
	buffer_load_dwordx4 v196, s[8:11], s14 offen lds
	s_waitcnt vmcnt(8)
	s_waitcnt lgkmcnt(8)
	s_barrier
	s_setprio 1
	s_waitcnt lgkmcnt(7)
	v_mfma_f32_16x16x32_bf16 v[124:127], v[156:159], v[160:163], v[124:127]
	s_waitcnt lgkmcnt(6)
	v_mfma_f32_16x16x32_bf16 v[124:127], v[152:155], v[164:167], v[124:127]
	v_mfma_f32_16x16x32_bf16 v[120:123], v[148:151], v[160:163], v[120:123]
	s_nop 0
	v_mfma_f32_16x16x32_bf16 v[120:123], v[144:147], v[164:167], v[120:123]
	s_waitcnt lgkmcnt(5)
	v_mfma_f32_16x16x32_bf16 v[116:119], v[156:159], v[168:171], v[116:119]
	s_waitcnt lgkmcnt(4)
	v_mfma_f32_16x16x32_bf16 v[116:119], v[152:155], v[172:175], v[116:119]
	v_mfma_f32_16x16x32_bf16 v[112:115], v[148:151], v[168:171], v[112:115]
	s_nop 0
	v_mfma_f32_16x16x32_bf16 v[112:115], v[144:147], v[172:175], v[112:115]
	s_waitcnt lgkmcnt(3)
	v_mfma_f32_16x16x32_bf16 v[108:111], v[156:159], v[176:179], v[108:111]
	s_waitcnt lgkmcnt(2)
	v_mfma_f32_16x16x32_bf16 v[108:111], v[152:155], v[180:183], v[108:111]
	v_mfma_f32_16x16x32_bf16 v[104:107], v[148:151], v[176:179], v[104:107]
	s_nop 0
	v_mfma_f32_16x16x32_bf16 v[104:107], v[144:147], v[180:183], v[104:107]
	s_waitcnt lgkmcnt(1)
	v_mfma_f32_16x16x32_bf16 v[100:103], v[156:159], v[184:187], v[100:103]
	s_waitcnt lgkmcnt(0)
	v_mfma_f32_16x16x32_bf16 v[100:103], v[152:155], v[188:191], v[100:103]
	v_mfma_f32_16x16x32_bf16 v[96:99], v[148:151], v[184:187], v[96:99]
	s_nop 0
	v_mfma_f32_16x16x32_bf16 v[96:99], v[144:147], v[188:191], v[96:99]
	s_setprio 0
	s_setprio 1
	v_mfma_f32_16x16x32_bf16 v[92:95], v[140:143], v[160:163], v[92:95]
	s_nop 0
	v_mfma_f32_16x16x32_bf16 v[92:95], v[136:139], v[164:167], v[92:95]
	v_mfma_f32_16x16x32_bf16 v[88:91], v[132:135], v[160:163], v[88:91]
	s_nop 0
	v_mfma_f32_16x16x32_bf16 v[88:91], v[128:131], v[164:167], v[88:91]
	v_mfma_f32_16x16x32_bf16 v[84:87], v[140:143], v[168:171], v[84:87]
	s_nop 0
	v_mfma_f32_16x16x32_bf16 v[84:87], v[136:139], v[172:175], v[84:87]
	v_mfma_f32_16x16x32_bf16 v[80:83], v[132:135], v[168:171], v[80:83]
	s_nop 0
	v_mfma_f32_16x16x32_bf16 v[80:83], v[128:131], v[172:175], v[80:83]
	v_mfma_f32_16x16x32_bf16 v[76:79], v[140:143], v[176:179], v[76:79]
	s_nop 0
	v_mfma_f32_16x16x32_bf16 v[76:79], v[136:139], v[180:183], v[76:79]
	v_mfma_f32_16x16x32_bf16 v[72:75], v[132:135], v[176:179], v[72:75]
	s_nop 0
	v_mfma_f32_16x16x32_bf16 v[72:75], v[128:131], v[180:183], v[72:75]
	v_mfma_f32_16x16x32_bf16 v[68:71], v[140:143], v[184:187], v[68:71]
	s_nop 0
	v_mfma_f32_16x16x32_bf16 v[68:71], v[136:139], v[188:191], v[68:71]
	v_mfma_f32_16x16x32_bf16 v[64:67], v[132:135], v[184:187], v[64:67]
	s_nop 0
	v_mfma_f32_16x16x32_bf16 v[64:67], v[128:131], v[188:191], v[64:67]
	s_setprio 0
	s_barrier
	ds_read_b128 v[160:163], v219 offset:49152
	ds_read_b128 v[164:167], v219 offset:50176
	ds_read_b128 v[168:171], v219 offset:51200
	ds_read_b128 v[172:175], v219 offset:52224
	ds_read_b128 v[176:179], v219 offset:53248
	ds_read_b128 v[180:183], v219 offset:54272
	ds_read_b128 v[184:187], v219 offset:55296
	ds_read_b128 v[188:191], v219 offset:56320
	s_mov_b32 m0, s73
	s_mov_b32 s14, s10
	s_mov_b32 s15, s11
	buffer_load_dwordx4 v202, s[12:15], s5 offen lds
	s_add_i32 s5, s93, 0x80180
	s_mov_b32 m0, s74
	s_nop 0
	buffer_load_dwordx4 v202, s[12:15], s5 offen lds
	s_add_i32 s5, s93, 0x8180
	s_mov_b32 m0, s77
	s_nop 0
	buffer_load_dwordx4 v202, s[12:15], s5 offen lds
	s_add_i32 s5, s93, 0x88180
	s_mov_b32 m0, s78
	s_nop 0
	buffer_load_dwordx4 v202, s[12:15], s5 offen lds
	s_mov_b32 m0, s75
	s_nop 0
	buffer_load_dwordx4 v196, s[8:11], s4 offen lds
	s_add_i32 s4, s92, 0x10180
	s_mov_b32 m0, s76
	s_nop 0
	buffer_load_dwordx4 v196, s[8:11], s4 offen lds
	s_waitcnt vmcnt(8)
	s_waitcnt lgkmcnt(6)
	s_barrier
	s_setprio 1
	v_mfma_f32_16x16x32_bf16 v[60:63], v[156:159], v[160:163], v[60:63]
	v_mfma_f32_16x16x32_bf16 v[60:63], v[152:155], v[164:167], v[60:63]
	v_mfma_f32_16x16x32_bf16 v[56:59], v[148:151], v[160:163], v[56:59]
	s_nop 0
	v_mfma_f32_16x16x32_bf16 v[56:59], v[144:147], v[164:167], v[56:59]
	s_waitcnt lgkmcnt(5)
	v_mfma_f32_16x16x32_bf16 v[52:55], v[156:159], v[168:171], v[52:55]
	s_waitcnt lgkmcnt(4)
	v_mfma_f32_16x16x32_bf16 v[52:55], v[152:155], v[172:175], v[52:55]
	v_mfma_f32_16x16x32_bf16 v[48:51], v[148:151], v[168:171], v[48:51]
	s_nop 0
	v_mfma_f32_16x16x32_bf16 v[48:51], v[144:147], v[172:175], v[48:51]
	s_waitcnt lgkmcnt(3)
	v_mfma_f32_16x16x32_bf16 v[44:47], v[156:159], v[176:179], v[44:47]
	s_waitcnt lgkmcnt(2)
	v_mfma_f32_16x16x32_bf16 v[44:47], v[152:155], v[180:183], v[44:47]
	v_mfma_f32_16x16x32_bf16 v[40:43], v[148:151], v[176:179], v[40:43]
	s_nop 0
	v_mfma_f32_16x16x32_bf16 v[40:43], v[144:147], v[180:183], v[40:43]
	s_waitcnt lgkmcnt(1)
	v_mfma_f32_16x16x32_bf16 v[36:39], v[156:159], v[184:187], v[36:39]
	s_waitcnt lgkmcnt(0)
	v_mfma_f32_16x16x32_bf16 v[36:39], v[152:155], v[188:191], v[36:39]
	v_mfma_f32_16x16x32_bf16 v[32:35], v[148:151], v[184:187], v[32:35]
	s_nop 0
	v_mfma_f32_16x16x32_bf16 v[32:35], v[144:147], v[188:191], v[32:35]
	s_setprio 0
	s_setprio 1
	v_mfma_f32_16x16x32_bf16 v[28:31], v[140:143], v[160:163], v[28:31]
	s_nop 0
	v_mfma_f32_16x16x32_bf16 v[28:31], v[136:139], v[164:167], v[28:31]
	v_mfma_f32_16x16x32_bf16 v[24:27], v[132:135], v[160:163], v[24:27]
	s_nop 0
	v_mfma_f32_16x16x32_bf16 v[24:27], v[128:131], v[164:167], v[24:27]
	v_mfma_f32_16x16x32_bf16 v[20:23], v[140:143], v[168:171], v[20:23]
	s_nop 0
	v_mfma_f32_16x16x32_bf16 v[20:23], v[136:139], v[172:175], v[20:23]
	v_mfma_f32_16x16x32_bf16 v[16:19], v[132:135], v[168:171], v[16:19]
	s_nop 0
	v_mfma_f32_16x16x32_bf16 v[16:19], v[128:131], v[172:175], v[16:19]
	v_mfma_f32_16x16x32_bf16 v[12:15], v[140:143], v[176:179], v[12:15]
	s_nop 0
	v_mfma_f32_16x16x32_bf16 v[12:15], v[136:139], v[180:183], v[12:15]
	v_mfma_f32_16x16x32_bf16 v[8:11], v[132:135], v[176:179], v[8:11]
	s_nop 0
	v_mfma_f32_16x16x32_bf16 v[8:11], v[128:131], v[180:183], v[8:11]
	v_mfma_f32_16x16x32_bf16 v[4:7], v[140:143], v[184:187], v[4:7]
	s_nop 0
	v_mfma_f32_16x16x32_bf16 v[4:7], v[136:139], v[188:191], v[4:7]
	v_mfma_f32_16x16x32_bf16 v[0:3], v[132:135], v[184:187], v[0:3]
	s_nop 0
	v_mfma_f32_16x16x32_bf16 v[0:3], v[128:131], v[188:191], v[0:3]
	s_setprio 0
	s_barrier
	s_add_i32 s4, s92, 0x30180
	s_add_i32 s5, s93, 0x200
	s_mov_b32 s33, 0
.LBB0_220:
	ds_read_b128 v[128:131], v203
	ds_read_b128 v[132:135], v204
	ds_read_b128 v[136:139], v205
	ds_read_b128 v[140:143], v206
	ds_read_b128 v[144:147], v207
	ds_read_b128 v[148:151], v208
	ds_read_b128 v[152:155], v209
	ds_read_b128 v[156:159], v210
	ds_read_b128 v[160:163], v219
	ds_read_b128 v[164:167], v219 offset:1024
	ds_read_b128 v[168:171], v219 offset:2048
	ds_read_b128 v[172:175], v219 offset:3072
	ds_read_b128 v[176:179], v219 offset:4096
	ds_read_b128 v[180:183], v219 offset:5120
	ds_read_b128 v[184:187], v219 offset:6144
	ds_read_b128 v[188:191], v219 offset:7168
	s_add_i32 s66, s4, 0xfffd0080
	s_cmp_eq_u32 s33, 4
	s_cselect_b32 s66, s90, s66
	s_cselect_b32 s92, s91, s5
	s_add_i32 s67, s66, 0x80
	s_mov_b32 m0, s79
	s_add_i32 s93, s4, 0xffff0000
	buffer_load_dwordx4 v196, s[8:11], s93 offen lds
	s_mov_b32 m0, s81
	s_nop 0
	buffer_load_dwordx4 v196, s[8:11], s4 offen lds
	s_waitcnt vmcnt(8)
	s_waitcnt lgkmcnt(8)
	s_barrier
	s_setprio 1
	s_waitcnt lgkmcnt(7)
	v_mfma_f32_16x16x32_bf16 v[124:127], v[128:131], v[160:163], v[124:127]
	s_waitcnt lgkmcnt(6)
	v_mfma_f32_16x16x32_bf16 v[124:127], v[132:135], v[164:167], v[124:127]
	v_mfma_f32_16x16x32_bf16 v[120:123], v[136:139], v[160:163], v[120:123]
	s_nop 0
	v_mfma_f32_16x16x32_bf16 v[120:123], v[140:143], v[164:167], v[120:123]
	s_waitcnt lgkmcnt(5)
	v_mfma_f32_16x16x32_bf16 v[116:119], v[128:131], v[168:171], v[116:119]
	s_waitcnt lgkmcnt(4)
	v_mfma_f32_16x16x32_bf16 v[116:119], v[132:135], v[172:175], v[116:119]
	v_mfma_f32_16x16x32_bf16 v[112:115], v[136:139], v[168:171], v[112:115]
	s_nop 0
	v_mfma_f32_16x16x32_bf16 v[112:115], v[140:143], v[172:175], v[112:115]
	s_waitcnt lgkmcnt(3)
	v_mfma_f32_16x16x32_bf16 v[108:111], v[128:131], v[176:179], v[108:111]
	s_waitcnt lgkmcnt(2)
	v_mfma_f32_16x16x32_bf16 v[108:111], v[132:135], v[180:183], v[108:111]
	v_mfma_f32_16x16x32_bf16 v[104:107], v[136:139], v[176:179], v[104:107]
	s_nop 0
	v_mfma_f32_16x16x32_bf16 v[104:107], v[140:143], v[180:183], v[104:107]
	s_waitcnt lgkmcnt(1)
	v_mfma_f32_16x16x32_bf16 v[100:103], v[128:131], v[184:187], v[100:103]
	s_waitcnt lgkmcnt(0)
	v_mfma_f32_16x16x32_bf16 v[100:103], v[132:135], v[188:191], v[100:103]
	v_mfma_f32_16x16x32_bf16 v[96:99], v[136:139], v[184:187], v[96:99]
	s_nop 0
	v_mfma_f32_16x16x32_bf16 v[96:99], v[140:143], v[188:191], v[96:99]
	s_setprio 0
	s_setprio 1
	v_mfma_f32_16x16x32_bf16 v[92:95], v[144:147], v[160:163], v[92:95]
	s_nop 0
	v_mfma_f32_16x16x32_bf16 v[92:95], v[148:151], v[164:167], v[92:95]
	v_mfma_f32_16x16x32_bf16 v[88:91], v[152:155], v[160:163], v[88:91]
	s_nop 0
	v_mfma_f32_16x16x32_bf16 v[88:91], v[156:159], v[164:167], v[88:91]
	v_mfma_f32_16x16x32_bf16 v[84:87], v[144:147], v[168:171], v[84:87]
	s_nop 0
	v_mfma_f32_16x16x32_bf16 v[84:87], v[148:151], v[172:175], v[84:87]
	v_mfma_f32_16x16x32_bf16 v[80:83], v[152:155], v[168:171], v[80:83]
	s_nop 0
	v_mfma_f32_16x16x32_bf16 v[80:83], v[156:159], v[172:175], v[80:83]
	v_mfma_f32_16x16x32_bf16 v[76:79], v[144:147], v[176:179], v[76:79]
	s_nop 0
	v_mfma_f32_16x16x32_bf16 v[76:79], v[148:151], v[180:183], v[76:79]
	v_mfma_f32_16x16x32_bf16 v[72:75], v[152:155], v[176:179], v[72:75]
	s_nop 0
	v_mfma_f32_16x16x32_bf16 v[72:75], v[156:159], v[180:183], v[72:75]
	v_mfma_f32_16x16x32_bf16 v[68:71], v[144:147], v[184:187], v[68:71]
	s_nop 0
	v_mfma_f32_16x16x32_bf16 v[68:71], v[148:151], v[188:191], v[68:71]
	v_mfma_f32_16x16x32_bf16 v[64:67], v[152:155], v[184:187], v[64:67]
	s_nop 0
	v_mfma_f32_16x16x32_bf16 v[64:67], v[156:159], v[188:191], v[64:67]
	s_setprio 0
	s_barrier
	ds_read_b128 v[160:163], v219 offset:16384
	ds_read_b128 v[164:167], v219 offset:17408
	ds_read_b128 v[168:171], v219 offset:18432
	ds_read_b128 v[172:175], v219 offset:19456
	ds_read_b128 v[176:179], v219 offset:20480
	ds_read_b128 v[180:183], v219 offset:21504
	ds_read_b128 v[184:187], v219 offset:22528
	ds_read_b128 v[188:191], v219 offset:23552
	s_mov_b32 m0, s62
	s_add_i32 s93, s92, 0x80000
	buffer_load_dwordx4 v202, s[12:15], s92 offen lds
	s_mov_b32 m0, s63
	s_nop 0
	buffer_load_dwordx4 v202, s[12:15], s93 offen lds
	s_add_i32 s93, s92, 0x8000
	s_mov_b32 m0, s64
	s_nop 0
	buffer_load_dwordx4 v202, s[12:15], s93 offen lds
	s_add_i32 s93, s92, 0x88000
	s_mov_b32 m0, s65
	s_nop 0
	buffer_load_dwordx4 v202, s[12:15], s93 offen lds
	s_mov_b32 m0, s45
	s_add_i32 s93, s66, 0x10000
	buffer_load_dwordx4 v196, s[8:11], s66 offen lds
	s_mov_b32 m0, s68
	s_nop 0
	buffer_load_dwordx4 v196, s[8:11], s93 offen lds
	s_waitcnt vmcnt(8)
	s_waitcnt lgkmcnt(6)
	s_barrier
	s_setprio 1
	v_mfma_f32_16x16x32_bf16 v[60:63], v[128:131], v[160:163], v[60:63]
	v_mfma_f32_16x16x32_bf16 v[60:63], v[132:135], v[164:167], v[60:63]
	v_mfma_f32_16x16x32_bf16 v[56:59], v[136:139], v[160:163], v[56:59]
	s_nop 0
	v_mfma_f32_16x16x32_bf16 v[56:59], v[140:143], v[164:167], v[56:59]
	s_waitcnt lgkmcnt(5)
	v_mfma_f32_16x16x32_bf16 v[52:55], v[128:131], v[168:171], v[52:55]
	s_waitcnt lgkmcnt(4)
	v_mfma_f32_16x16x32_bf16 v[52:55], v[132:135], v[172:175], v[52:55]
	v_mfma_f32_16x16x32_bf16 v[48:51], v[136:139], v[168:171], v[48:51]
	s_nop 0
	v_mfma_f32_16x16x32_bf16 v[48:51], v[140:143], v[172:175], v[48:51]
	s_waitcnt lgkmcnt(3)
	v_mfma_f32_16x16x32_bf16 v[44:47], v[128:131], v[176:179], v[44:47]
	s_waitcnt lgkmcnt(2)
	v_mfma_f32_16x16x32_bf16 v[44:47], v[132:135], v[180:183], v[44:47]
	v_mfma_f32_16x16x32_bf16 v[40:43], v[136:139], v[176:179], v[40:43]
	s_nop 0
	v_mfma_f32_16x16x32_bf16 v[40:43], v[140:143], v[180:183], v[40:43]
	s_waitcnt lgkmcnt(1)
	v_mfma_f32_16x16x32_bf16 v[36:39], v[128:131], v[184:187], v[36:39]
	s_waitcnt lgkmcnt(0)
	v_mfma_f32_16x16x32_bf16 v[36:39], v[132:135], v[188:191], v[36:39]
	v_mfma_f32_16x16x32_bf16 v[32:35], v[136:139], v[184:187], v[32:35]
	s_nop 0
	v_mfma_f32_16x16x32_bf16 v[32:35], v[140:143], v[188:191], v[32:35]
	s_setprio 0
	s_setprio 1
	v_mfma_f32_16x16x32_bf16 v[28:31], v[144:147], v[160:163], v[28:31]
	s_nop 0
	v_mfma_f32_16x16x32_bf16 v[28:31], v[148:151], v[164:167], v[28:31]
	v_mfma_f32_16x16x32_bf16 v[24:27], v[152:155], v[160:163], v[24:27]
	s_nop 0
	v_mfma_f32_16x16x32_bf16 v[24:27], v[156:159], v[164:167], v[24:27]
	v_mfma_f32_16x16x32_bf16 v[20:23], v[144:147], v[168:171], v[20:23]
	s_nop 0
	v_mfma_f32_16x16x32_bf16 v[20:23], v[148:151], v[172:175], v[20:23]
	v_mfma_f32_16x16x32_bf16 v[16:19], v[152:155], v[168:171], v[16:19]
	s_nop 0
	v_mfma_f32_16x16x32_bf16 v[16:19], v[156:159], v[172:175], v[16:19]
	v_mfma_f32_16x16x32_bf16 v[12:15], v[144:147], v[176:179], v[12:15]
	s_nop 0
	v_mfma_f32_16x16x32_bf16 v[12:15], v[148:151], v[180:183], v[12:15]
	v_mfma_f32_16x16x32_bf16 v[8:11], v[152:155], v[176:179], v[8:11]
	s_nop 0
	v_mfma_f32_16x16x32_bf16 v[8:11], v[156:159], v[180:183], v[8:11]
	v_mfma_f32_16x16x32_bf16 v[4:7], v[144:147], v[184:187], v[4:7]
	s_nop 0
	v_mfma_f32_16x16x32_bf16 v[4:7], v[148:151], v[188:191], v[4:7]
	v_mfma_f32_16x16x32_bf16 v[0:3], v[152:155], v[184:187], v[0:3]
	s_nop 0
	v_mfma_f32_16x16x32_bf16 v[0:3], v[156:159], v[188:191], v[0:3]
	s_setprio 0
	s_barrier
	ds_read_b128 v[140:143], v211
	ds_read_b128 v[144:147], v212
	ds_read_b128 v[148:151], v213
	ds_read_b128 v[152:155], v214
	ds_read_b128 v[156:159], v215
	ds_read_b128 v[136:139], v216
	ds_read_b128 v[132:135], v217
	ds_read_b128 v[128:131], v218
	ds_read_b128 v[160:163], v219 offset:32768
	ds_read_b128 v[164:167], v219 offset:33792
	ds_read_b128 v[168:171], v219 offset:34816
	ds_read_b128 v[172:175], v219 offset:35840
	ds_read_b128 v[176:179], v219 offset:36864
	ds_read_b128 v[180:183], v219 offset:37888
	ds_read_b128 v[184:187], v219 offset:38912
	ds_read_b128 v[188:191], v219 offset:39936
	s_mov_b32 m0, s69
	s_add_i32 s93, s66, 0x20000
	buffer_load_dwordx4 v196, s[8:11], s93 offen lds
	s_add_i32 s93, s66, 0x30000
	s_mov_b32 m0, s70
	s_nop 0
	buffer_load_dwordx4 v196, s[8:11], s93 offen lds
	s_waitcnt vmcnt(8)
	s_waitcnt lgkmcnt(8)
	s_barrier
	s_setprio 1
	s_waitcnt lgkmcnt(7)
	v_mfma_f32_16x16x32_bf16 v[124:127], v[140:143], v[160:163], v[124:127]
	s_waitcnt lgkmcnt(6)
	v_mfma_f32_16x16x32_bf16 v[124:127], v[144:147], v[164:167], v[124:127]
	v_mfma_f32_16x16x32_bf16 v[120:123], v[148:151], v[160:163], v[120:123]
	s_nop 0
	v_mfma_f32_16x16x32_bf16 v[120:123], v[152:155], v[164:167], v[120:123]
	s_waitcnt lgkmcnt(5)
	v_mfma_f32_16x16x32_bf16 v[116:119], v[140:143], v[168:171], v[116:119]
	s_waitcnt lgkmcnt(4)
	v_mfma_f32_16x16x32_bf16 v[116:119], v[144:147], v[172:175], v[116:119]
	v_mfma_f32_16x16x32_bf16 v[112:115], v[148:151], v[168:171], v[112:115]
	s_nop 0
	v_mfma_f32_16x16x32_bf16 v[112:115], v[152:155], v[172:175], v[112:115]
	s_waitcnt lgkmcnt(3)
	v_mfma_f32_16x16x32_bf16 v[108:111], v[140:143], v[176:179], v[108:111]
	s_waitcnt lgkmcnt(2)
	v_mfma_f32_16x16x32_bf16 v[108:111], v[144:147], v[180:183], v[108:111]
	v_mfma_f32_16x16x32_bf16 v[104:107], v[148:151], v[176:179], v[104:107]
	s_nop 0
	v_mfma_f32_16x16x32_bf16 v[104:107], v[152:155], v[180:183], v[104:107]
	s_waitcnt lgkmcnt(1)
	v_mfma_f32_16x16x32_bf16 v[100:103], v[140:143], v[184:187], v[100:103]
	s_waitcnt lgkmcnt(0)
	v_mfma_f32_16x16x32_bf16 v[100:103], v[144:147], v[188:191], v[100:103]
	v_mfma_f32_16x16x32_bf16 v[96:99], v[148:151], v[184:187], v[96:99]
	s_nop 0
	v_mfma_f32_16x16x32_bf16 v[96:99], v[152:155], v[188:191], v[96:99]
	s_setprio 0
	s_setprio 1
	v_mfma_f32_16x16x32_bf16 v[92:95], v[156:159], v[160:163], v[92:95]
	s_nop 0
	v_mfma_f32_16x16x32_bf16 v[92:95], v[136:139], v[164:167], v[92:95]
	v_mfma_f32_16x16x32_bf16 v[88:91], v[132:135], v[160:163], v[88:91]
	s_nop 0
	v_mfma_f32_16x16x32_bf16 v[88:91], v[128:131], v[164:167], v[88:91]
	v_mfma_f32_16x16x32_bf16 v[84:87], v[156:159], v[168:171], v[84:87]
	s_nop 0
	v_mfma_f32_16x16x32_bf16 v[84:87], v[136:139], v[172:175], v[84:87]
	v_mfma_f32_16x16x32_bf16 v[80:83], v[132:135], v[168:171], v[80:83]
	s_nop 0
	v_mfma_f32_16x16x32_bf16 v[80:83], v[128:131], v[172:175], v[80:83]
	v_mfma_f32_16x16x32_bf16 v[76:79], v[156:159], v[176:179], v[76:79]
	s_nop 0
	v_mfma_f32_16x16x32_bf16 v[76:79], v[136:139], v[180:183], v[76:79]
	v_mfma_f32_16x16x32_bf16 v[72:75], v[132:135], v[176:179], v[72:75]
	s_nop 0
	v_mfma_f32_16x16x32_bf16 v[72:75], v[128:131], v[180:183], v[72:75]
	v_mfma_f32_16x16x32_bf16 v[68:71], v[156:159], v[184:187], v[68:71]
	s_nop 0
	v_mfma_f32_16x16x32_bf16 v[68:71], v[136:139], v[188:191], v[68:71]
	v_mfma_f32_16x16x32_bf16 v[64:67], v[132:135], v[184:187], v[64:67]
	s_nop 0
	v_mfma_f32_16x16x32_bf16 v[64:67], v[128:131], v[188:191], v[64:67]
	s_setprio 0
	s_barrier
	ds_read_b128 v[160:163], v219 offset:49152
	ds_read_b128 v[164:167], v219 offset:50176
	ds_read_b128 v[168:171], v219 offset:51200
	ds_read_b128 v[172:175], v219 offset:52224
	ds_read_b128 v[176:179], v219 offset:53248
	ds_read_b128 v[180:183], v219 offset:54272
	ds_read_b128 v[184:187], v219 offset:55296
	ds_read_b128 v[188:191], v219 offset:56320
	s_mov_b32 m0, s73
	s_add_i32 s93, s92, 0x80
	buffer_load_dwordx4 v202, s[12:15], s93 offen lds
	s_add_i32 s93, s92, 0x80080
	s_mov_b32 m0, s74
	s_add_i32 s66, s66, 0x10080
	buffer_load_dwordx4 v202, s[12:15], s93 offen lds
	s_add_i32 s93, s92, 0x8080
	s_mov_b32 m0, s77
	s_add_i32 s92, s92, 0x88080
	buffer_load_dwordx4 v202, s[12:15], s93 offen lds
	s_mov_b32 m0, s78
	s_nop 0
	buffer_load_dwordx4 v202, s[12:15], s92 offen lds
	s_mov_b32 m0, s75
	s_nop 0
	buffer_load_dwordx4 v196, s[8:11], s67 offen lds
	s_mov_b32 m0, s76
	s_nop 0
	buffer_load_dwordx4 v196, s[8:11], s66 offen lds
	s_waitcnt vmcnt(8)
	s_waitcnt lgkmcnt(6)
	s_barrier
	s_setprio 1
	v_mfma_f32_16x16x32_bf16 v[60:63], v[140:143], v[160:163], v[60:63]
	v_mfma_f32_16x16x32_bf16 v[60:63], v[144:147], v[164:167], v[60:63]
	v_mfma_f32_16x16x32_bf16 v[56:59], v[148:151], v[160:163], v[56:59]
	s_nop 0
	v_mfma_f32_16x16x32_bf16 v[56:59], v[152:155], v[164:167], v[56:59]
	s_waitcnt lgkmcnt(5)
	v_mfma_f32_16x16x32_bf16 v[52:55], v[140:143], v[168:171], v[52:55]
	s_waitcnt lgkmcnt(4)
	v_mfma_f32_16x16x32_bf16 v[52:55], v[144:147], v[172:175], v[52:55]
	v_mfma_f32_16x16x32_bf16 v[48:51], v[148:151], v[168:171], v[48:51]
	s_nop 0
	v_mfma_f32_16x16x32_bf16 v[48:51], v[152:155], v[172:175], v[48:51]
	s_waitcnt lgkmcnt(3)
	v_mfma_f32_16x16x32_bf16 v[44:47], v[140:143], v[176:179], v[44:47]
	s_waitcnt lgkmcnt(2)
	v_mfma_f32_16x16x32_bf16 v[44:47], v[144:147], v[180:183], v[44:47]
	v_mfma_f32_16x16x32_bf16 v[40:43], v[148:151], v[176:179], v[40:43]
	s_nop 0
	v_mfma_f32_16x16x32_bf16 v[40:43], v[152:155], v[180:183], v[40:43]
	s_waitcnt lgkmcnt(1)
	v_mfma_f32_16x16x32_bf16 v[36:39], v[140:143], v[184:187], v[36:39]
	s_waitcnt lgkmcnt(0)
	v_mfma_f32_16x16x32_bf16 v[36:39], v[144:147], v[188:191], v[36:39]
	v_mfma_f32_16x16x32_bf16 v[32:35], v[148:151], v[184:187], v[32:35]
	s_nop 0
	v_mfma_f32_16x16x32_bf16 v[32:35], v[152:155], v[188:191], v[32:35]
	s_setprio 0
	s_setprio 1
	v_mfma_f32_16x16x32_bf16 v[28:31], v[156:159], v[160:163], v[28:31]
	s_nop 0
	v_mfma_f32_16x16x32_bf16 v[28:31], v[136:139], v[164:167], v[28:31]
	v_mfma_f32_16x16x32_bf16 v[24:27], v[132:135], v[160:163], v[24:27]
	s_nop 0
	v_mfma_f32_16x16x32_bf16 v[24:27], v[128:131], v[164:167], v[24:27]
	v_mfma_f32_16x16x32_bf16 v[20:23], v[156:159], v[168:171], v[20:23]
	s_nop 0
	v_mfma_f32_16x16x32_bf16 v[20:23], v[136:139], v[172:175], v[20:23]
	v_mfma_f32_16x16x32_bf16 v[16:19], v[132:135], v[168:171], v[16:19]
	s_nop 0
	v_mfma_f32_16x16x32_bf16 v[16:19], v[128:131], v[172:175], v[16:19]
	v_mfma_f32_16x16x32_bf16 v[12:15], v[156:159], v[176:179], v[12:15]
	s_nop 0
	v_mfma_f32_16x16x32_bf16 v[12:15], v[136:139], v[180:183], v[12:15]
	v_mfma_f32_16x16x32_bf16 v[8:11], v[132:135], v[176:179], v[8:11]
	s_nop 0
	v_mfma_f32_16x16x32_bf16 v[8:11], v[128:131], v[180:183], v[8:11]
	v_mfma_f32_16x16x32_bf16 v[4:7], v[156:159], v[184:187], v[4:7]
	s_nop 0
	v_mfma_f32_16x16x32_bf16 v[4:7], v[136:139], v[188:191], v[4:7]
	v_mfma_f32_16x16x32_bf16 v[0:3], v[132:135], v[184:187], v[0:3]
	s_nop 0
	v_mfma_f32_16x16x32_bf16 v[0:3], v[128:131], v[188:191], v[0:3]
	s_setprio 0
	s_barrier
	s_add_i32 s33, s33, 2
	s_addk_i32 s4, 0x100
	s_addk_i32 s5, 0x100
	s_cmp_gt_u32 s33, 5
	s_cbranch_scc0 .LBB0_220
	s_and_b64 vcc, exec, s[16:17]
	s_cbranch_vccz .LBB0_223
	s_barrier

.LBB0_253:
	s_waitcnt lgkmcnt(0)
	s_add_i32 s33, s91, 0x180
	s_add_i32 s42, s90, 0x180
	s_barrier
	s_setprio 1
	s_waitcnt lgkmcnt(7)
	v_mfma_f32_16x16x32_bf16 v[60:63], v[156:159], v[188:191], 0
	s_waitcnt lgkmcnt(6)
	v_mfma_f32_16x16x32_bf16 v[60:63], v[152:155], v[184:187], v[60:63]
	v_mfma_f32_16x16x32_bf16 v[56:59], v[148:151], v[188:191], 0
	s_nop 0
	v_mfma_f32_16x16x32_bf16 v[56:59], v[144:147], v[184:187], v[56:59]
	s_waitcnt lgkmcnt(5)
	v_mfma_f32_16x16x32_bf16 v[52:55], v[156:159], v[180:183], 0
	s_waitcnt lgkmcnt(4)
	v_mfma_f32_16x16x32_bf16 v[52:55], v[152:155], v[176:179], v[52:55]
	v_mfma_f32_16x16x32_bf16 v[48:51], v[148:151], v[180:183], 0
	s_nop 0
	v_mfma_f32_16x16x32_bf16 v[48:51], v[144:147], v[176:179], v[48:51]
	s_waitcnt lgkmcnt(3)
	v_mfma_f32_16x16x32_bf16 v[44:47], v[156:159], v[172:175], 0
	s_waitcnt lgkmcnt(2)
	v_mfma_f32_16x16x32_bf16 v[44:47], v[152:155], v[168:171], v[44:47]
	v_mfma_f32_16x16x32_bf16 v[40:43], v[148:151], v[172:175], 0
	s_nop 0
	v_mfma_f32_16x16x32_bf16 v[40:43], v[144:147], v[168:171], v[40:43]
	s_waitcnt lgkmcnt(1)
	v_mfma_f32_16x16x32_bf16 v[36:39], v[156:159], v[164:167], 0
	s_waitcnt lgkmcnt(0)
	v_mfma_f32_16x16x32_bf16 v[36:39], v[152:155], v[160:163], v[36:39]
	v_mfma_f32_16x16x32_bf16 v[32:35], v[148:151], v[164:167], 0
	s_nop 0
	v_mfma_f32_16x16x32_bf16 v[32:35], v[144:147], v[160:163], v[32:35]
	s_setprio 0
	s_setprio 1
	v_mfma_f32_16x16x32_bf16 v[28:31], v[140:143], v[188:191], 0
	s_nop 0
	v_mfma_f32_16x16x32_bf16 v[28:31], v[136:139], v[184:187], v[28:31]
	v_mfma_f32_16x16x32_bf16 v[24:27], v[132:135], v[188:191], 0
	s_nop 0
	v_mfma_f32_16x16x32_bf16 v[24:27], v[128:131], v[184:187], v[24:27]
	v_mfma_f32_16x16x32_bf16 v[20:23], v[140:143], v[180:183], 0
	s_nop 0
	v_mfma_f32_16x16x32_bf16 v[20:23], v[136:139], v[176:179], v[20:23]
	v_mfma_f32_16x16x32_bf16 v[16:19], v[132:135], v[180:183], 0
	s_nop 0
	v_mfma_f32_16x16x32_bf16 v[16:19], v[128:131], v[176:179], v[16:19]
	v_mfma_f32_16x16x32_bf16 v[12:15], v[140:143], v[172:175], 0
	s_nop 0
	v_mfma_f32_16x16x32_bf16 v[12:15], v[136:139], v[168:171], v[12:15]
	v_mfma_f32_16x16x32_bf16 v[8:11], v[132:135], v[172:175], 0
	s_nop 0
	v_mfma_f32_16x16x32_bf16 v[8:11], v[128:131], v[168:171], v[8:11]
	v_mfma_f32_16x16x32_bf16 v[4:7], v[140:143], v[164:167], 0
	s_nop 0
	v_mfma_f32_16x16x32_bf16 v[4:7], v[136:139], v[160:163], v[4:7]
	v_mfma_f32_16x16x32_bf16 v[0:3], v[132:135], v[164:167], 0
	s_nop 0
	v_mfma_f32_16x16x32_bf16 v[0:3], v[128:131], v[160:163], v[0:3]
	s_setprio 0
	s_barrier
	ds_read_b128 v[156:159], v203
	ds_read_b128 v[152:155], v204
	ds_read_b128 v[148:151], v205
	ds_read_b128 v[144:147], v206
	ds_read_b128 v[140:143], v207
	ds_read_b128 v[136:139], v208
	ds_read_b128 v[132:135], v209
	ds_read_b128 v[128:131], v210
	ds_read_b128 v[160:163], v197 offset:32768
	ds_read_b128 v[164:167], v197 offset:33792
	ds_read_b128 v[168:171], v197 offset:34816
	ds_read_b128 v[172:175], v197 offset:35840
	ds_read_b128 v[176:179], v197 offset:36864
	ds_read_b128 v[180:183], v197 offset:37888
	ds_read_b128 v[184:187], v197 offset:38912
	ds_read_b128 v[188:191], v197 offset:39936
	s_mov_b32 m0, s69
	s_add_i32 s10, s91, 0x20100
	buffer_load_dwordx4 v196, s[4:7], s10 offen lds
	s_add_i32 s10, s91, 0x30100
	s_mov_b32 m0, s70
	s_nop 0
	buffer_load_dwordx4 v196, s[4:7], s10 offen lds
	s_waitcnt vmcnt(8)
	s_waitcnt lgkmcnt(8)
	s_barrier
	s_setprio 1
	s_waitcnt lgkmcnt(7)
	v_mfma_f32_16x16x32_bf16 v[124:127], v[156:159], v[160:163], v[124:127]
	s_waitcnt lgkmcnt(6)
	v_mfma_f32_16x16x32_bf16 v[124:127], v[152:155], v[164:167], v[124:127]
	v_mfma_f32_16x16x32_bf16 v[120:123], v[148:151], v[160:163], v[120:123]
	s_nop 0
	v_mfma_f32_16x16x32_bf16 v[120:123], v[144:147], v[164:167], v[120:123]
	s_waitcnt lgkmcnt(5)
	v_mfma_f32_16x16x32_bf16 v[116:119], v[156:159], v[168:171], v[116:119]
	s_waitcnt lgkmcnt(4)
	v_mfma_f32_16x16x32_bf16 v[116:119], v[152:155], v[172:175], v[116:119]
	v_mfma_f32_16x16x32_bf16 v[112:115], v[148:151], v[168:171], v[112:115]
	s_nop 0
	v_mfma_f32_16x16x32_bf16 v[112:115], v[144:147], v[172:175], v[112:115]
	s_waitcnt lgkmcnt(3)
	v_mfma_f32_16x16x32_bf16 v[108:111], v[156:159], v[176:179], v[108:111]
	s_waitcnt lgkmcnt(2)
	v_mfma_f32_16x16x32_bf16 v[108:111], v[152:155], v[180:183], v[108:111]
	v_mfma_f32_16x16x32_bf16 v[104:107], v[148:151], v[176:179], v[104:107]
	s_nop 0
	v_mfma_f32_16x16x32_bf16 v[104:107], v[144:147], v[180:183], v[104:107]
	s_waitcnt lgkmcnt(1)
	v_mfma_f32_16x16x32_bf16 v[100:103], v[156:159], v[184:187], v[100:103]
	s_waitcnt lgkmcnt(0)
	v_mfma_f32_16x16x32_bf16 v[100:103], v[152:155], v[188:191], v[100:103]
	v_mfma_f32_16x16x32_bf16 v[96:99], v[148:151], v[184:187], v[96:99]
	s_nop 0
	v_mfma_f32_16x16x32_bf16 v[96:99], v[144:147], v[188:191], v[96:99]
	s_setprio 0
	s_setprio 1
	v_mfma_f32_16x16x32_bf16 v[92:95], v[140:143], v[160:163], v[92:95]
	s_nop 0
	v_mfma_f32_16x16x32_bf16 v[92:95], v[136:139], v[164:167], v[92:95]
	v_mfma_f32_16x16x32_bf16 v[88:91], v[132:135], v[160:163], v[88:91]
	s_nop 0
	v_mfma_f32_16x16x32_bf16 v[88:91], v[128:131], v[164:167], v[88:91]
	v_mfma_f32_16x16x32_bf16 v[84:87], v[140:143], v[168:171], v[84:87]
	s_nop 0
	v_mfma_f32_16x16x32_bf16 v[84:87], v[136:139], v[172:175], v[84:87]
	v_mfma_f32_16x16x32_bf16 v[80:83], v[132:135], v[168:171], v[80:83]
	s_nop 0
	v_mfma_f32_16x16x32_bf16 v[80:83], v[128:131], v[172:175], v[80:83]
	v_mfma_f32_16x16x32_bf16 v[76:79], v[140:143], v[176:179], v[76:79]
	s_nop 0
	v_mfma_f32_16x16x32_bf16 v[76:79], v[136:139], v[180:183], v[76:79]
	v_mfma_f32_16x16x32_bf16 v[72:75], v[132:135], v[176:179], v[72:75]
	s_nop 0
	v_mfma_f32_16x16x32_bf16 v[72:75], v[128:131], v[180:183], v[72:75]
	v_mfma_f32_16x16x32_bf16 v[68:71], v[140:143], v[184:187], v[68:71]
	s_nop 0
	v_mfma_f32_16x16x32_bf16 v[68:71], v[136:139], v[188:191], v[68:71]
	v_mfma_f32_16x16x32_bf16 v[64:67], v[132:135], v[184:187], v[64:67]
	s_nop 0
	v_mfma_f32_16x16x32_bf16 v[64:67], v[128:131], v[188:191], v[64:67]
	s_setprio 0
	s_barrier
	ds_read_b128 v[160:163], v197 offset:49152
	ds_read_b128 v[164:167], v197 offset:50176
	ds_read_b128 v[168:171], v197 offset:51200
	ds_read_b128 v[172:175], v197 offset:52224
	ds_read_b128 v[176:179], v197 offset:53248
	ds_read_b128 v[180:183], v197 offset:54272
	ds_read_b128 v[184:187], v197 offset:55296
	ds_read_b128 v[188:191], v197 offset:56320
	s_mov_b32 m0, s72
	s_mov_b32 s10, s6
	s_mov_b32 s11, s7
	buffer_load_dwordx4 v192, s[8:11], s42 offen lds
	s_add_i32 s42, s90, 0x20180
	s_mov_b32 m0, s73
	s_nop 0
	buffer_load_dwordx4 v192, s[8:11], s42 offen lds
	s_add_i32 s42, s90, 0x2180
	s_mov_b32 m0, s76
	s_nop 0
	buffer_load_dwordx4 v192, s[8:11], s42 offen lds
	s_add_i32 s42, s90, 0x22180
	s_mov_b32 m0, s77
	s_nop 0
	buffer_load_dwordx4 v192, s[8:11], s42 offen lds
	s_mov_b32 m0, s74
	s_nop 0
	buffer_load_dwordx4 v196, s[4:7], s33 offen lds
	s_add_i32 s33, s91, 0x10180
	s_mov_b32 m0, s75
	s_nop 0
	buffer_load_dwordx4 v196, s[4:7], s33 offen lds
	s_waitcnt vmcnt(8)
	s_waitcnt lgkmcnt(6)
	s_barrier
	s_setprio 1
	v_mfma_f32_16x16x32_bf16 v[60:63], v[156:159], v[160:163], v[60:63]
	v_mfma_f32_16x16x32_bf16 v[60:63], v[152:155], v[164:167], v[60:63]
	v_mfma_f32_16x16x32_bf16 v[56:59], v[148:151], v[160:163], v[56:59]
	s_nop 0
	v_mfma_f32_16x16x32_bf16 v[56:59], v[144:147], v[164:167], v[56:59]
	s_waitcnt lgkmcnt(5)
	v_mfma_f32_16x16x32_bf16 v[52:55], v[156:159], v[168:171], v[52:55]
	s_waitcnt lgkmcnt(4)
	v_mfma_f32_16x16x32_bf16 v[52:55], v[152:155], v[172:175], v[52:55]
	v_mfma_f32_16x16x32_bf16 v[48:51], v[148:151], v[168:171], v[48:51]
	s_nop 0
	v_mfma_f32_16x16x32_bf16 v[48:51], v[144:147], v[172:175], v[48:51]
	s_waitcnt lgkmcnt(3)
	v_mfma_f32_16x16x32_bf16 v[44:47], v[156:159], v[176:179], v[44:47]
	s_waitcnt lgkmcnt(2)
	v_mfma_f32_16x16x32_bf16 v[44:47], v[152:155], v[180:183], v[44:47]
	v_mfma_f32_16x16x32_bf16 v[40:43], v[148:151], v[176:179], v[40:43]
	s_nop 0
	v_mfma_f32_16x16x32_bf16 v[40:43], v[144:147], v[180:183], v[40:43]
	s_waitcnt lgkmcnt(1)
	v_mfma_f32_16x16x32_bf16 v[36:39], v[156:159], v[184:187], v[36:39]
	s_waitcnt lgkmcnt(0)
	v_mfma_f32_16x16x32_bf16 v[36:39], v[152:155], v[188:191], v[36:39]
	v_mfma_f32_16x16x32_bf16 v[32:35], v[148:151], v[184:187], v[32:35]
	s_nop 0
	v_mfma_f32_16x16x32_bf16 v[32:35], v[144:147], v[188:191], v[32:35]
	s_setprio 0
	s_setprio 1
	v_mfma_f32_16x16x32_bf16 v[28:31], v[140:143], v[160:163], v[28:31]
	s_nop 0
	v_mfma_f32_16x16x32_bf16 v[28:31], v[136:139], v[164:167], v[28:31]
	v_mfma_f32_16x16x32_bf16 v[24:27], v[132:135], v[160:163], v[24:27]
	s_nop 0
	v_mfma_f32_16x16x32_bf16 v[24:27], v[128:131], v[164:167], v[24:27]
	v_mfma_f32_16x16x32_bf16 v[20:23], v[140:143], v[168:171], v[20:23]
	s_nop 0
	v_mfma_f32_16x16x32_bf16 v[20:23], v[136:139], v[172:175], v[20:23]
	v_mfma_f32_16x16x32_bf16 v[16:19], v[132:135], v[168:171], v[16:19]
	s_nop 0
	v_mfma_f32_16x16x32_bf16 v[16:19], v[128:131], v[172:175], v[16:19]
	v_mfma_f32_16x16x32_bf16 v[12:15], v[140:143], v[176:179], v[12:15]
	s_nop 0
	v_mfma_f32_16x16x32_bf16 v[12:15], v[136:139], v[180:183], v[12:15]
	v_mfma_f32_16x16x32_bf16 v[8:11], v[132:135], v[176:179], v[8:11]
	s_nop 0
	v_mfma_f32_16x16x32_bf16 v[8:11], v[128:131], v[180:183], v[8:11]
	v_mfma_f32_16x16x32_bf16 v[4:7], v[140:143], v[184:187], v[4:7]
	s_nop 0
	v_mfma_f32_16x16x32_bf16 v[4:7], v[136:139], v[188:191], v[4:7]
	v_mfma_f32_16x16x32_bf16 v[0:3], v[132:135], v[184:187], v[0:3]
	s_nop 0
	v_mfma_f32_16x16x32_bf16 v[0:3], v[128:131], v[188:191], v[0:3]
	s_setprio 0
	s_barrier
	s_add_i32 s33, s91, 0x30180
	s_add_i32 s42, s90, 0x200
	s_mov_b32 s43, 0
.LBB0_254:
	ds_read_b128 v[128:131], v193
	ds_read_b128 v[132:135], v194
	ds_read_b128 v[136:139], v195
	ds_read_b128 v[140:143], v198
	ds_read_b128 v[144:147], v199
	ds_read_b128 v[148:151], v200
	ds_read_b128 v[152:155], v201
	ds_read_b128 v[156:159], v202
	ds_read_b128 v[160:163], v197
	ds_read_b128 v[164:167], v197 offset:1024
	ds_read_b128 v[168:171], v197 offset:2048
	ds_read_b128 v[172:175], v197 offset:3072
	ds_read_b128 v[176:179], v197 offset:4096
	ds_read_b128 v[180:183], v197 offset:5120
	ds_read_b128 v[184:187], v197 offset:6144
	ds_read_b128 v[188:191], v197 offset:7168
	s_add_i32 s66, s33, 0xfffd0080
	s_cmp_eq_u32 s43, 4
	s_cselect_b32 s66, s88, s66
	s_cselect_b32 s90, s89, s42
	s_add_i32 s67, s66, 0x80
	s_mov_b32 m0, s78
	s_add_i32 s91, s33, 0xffff0000
	buffer_load_dwordx4 v196, s[4:7], s91 offen lds
	s_mov_b32 m0, s79
	s_nop 0
	buffer_load_dwordx4 v196, s[4:7], s33 offen lds
	s_waitcnt vmcnt(8)
	s_waitcnt lgkmcnt(8)
	s_barrier
	s_setprio 1
	s_waitcnt lgkmcnt(7)
	v_mfma_f32_16x16x32_bf16 v[124:127], v[128:131], v[160:163], v[124:127]
	s_waitcnt lgkmcnt(6)
	v_mfma_f32_16x16x32_bf16 v[124:127], v[132:135], v[164:167], v[124:127]
	v_mfma_f32_16x16x32_bf16 v[120:123], v[136:139], v[160:163], v[120:123]
	s_nop 0
	v_mfma_f32_16x16x32_bf16 v[120:123], v[140:143], v[164:167], v[120:123]
	s_waitcnt lgkmcnt(5)
	v_mfma_f32_16x16x32_bf16 v[116:119], v[128:131], v[168:171], v[116:119]
	s_waitcnt lgkmcnt(4)
	v_mfma_f32_16x16x32_bf16 v[116:119], v[132:135], v[172:175], v[116:119]
	v_mfma_f32_16x16x32_bf16 v[112:115], v[136:139], v[168:171], v[112:115]
	s_nop 0
	v_mfma_f32_16x16x32_bf16 v[112:115], v[140:143], v[172:175], v[112:115]
	s_waitcnt lgkmcnt(3)
	v_mfma_f32_16x16x32_bf16 v[108:111], v[128:131], v[176:179], v[108:111]
	s_waitcnt lgkmcnt(2)
	v_mfma_f32_16x16x32_bf16 v[108:111], v[132:135], v[180:183], v[108:111]
	v_mfma_f32_16x16x32_bf16 v[104:107], v[136:139], v[176:179], v[104:107]
	s_nop 0
	v_mfma_f32_16x16x32_bf16 v[104:107], v[140:143], v[180:183], v[104:107]
	s_waitcnt lgkmcnt(1)
	v_mfma_f32_16x16x32_bf16 v[100:103], v[128:131], v[184:187], v[100:103]
	s_waitcnt lgkmcnt(0)
	v_mfma_f32_16x16x32_bf16 v[100:103], v[132:135], v[188:191], v[100:103]
	v_mfma_f32_16x16x32_bf16 v[96:99], v[136:139], v[184:187], v[96:99]
	s_nop 0
	v_mfma_f32_16x16x32_bf16 v[96:99], v[140:143], v[188:191], v[96:99]
	s_setprio 0
	s_setprio 1
	v_mfma_f32_16x16x32_bf16 v[92:95], v[144:147], v[160:163], v[92:95]
	s_nop 0
	v_mfma_f32_16x16x32_bf16 v[92:95], v[148:151], v[164:167], v[92:95]
	v_mfma_f32_16x16x32_bf16 v[88:91], v[152:155], v[160:163], v[88:91]
	s_nop 0
	v_mfma_f32_16x16x32_bf16 v[88:91], v[156:159], v[164:167], v[88:91]
	v_mfma_f32_16x16x32_bf16 v[84:87], v[144:147], v[168:171], v[84:87]
	s_nop 0
	v_mfma_f32_16x16x32_bf16 v[84:87], v[148:151], v[172:175], v[84:87]
	v_mfma_f32_16x16x32_bf16 v[80:83], v[152:155], v[168:171], v[80:83]
	s_nop 0
	v_mfma_f32_16x16x32_bf16 v[80:83], v[156:159], v[172:175], v[80:83]
	v_mfma_f32_16x16x32_bf16 v[76:79], v[144:147], v[176:179], v[76:79]
	s_nop 0
	v_mfma_f32_16x16x32_bf16 v[76:79], v[148:151], v[180:183], v[76:79]
	v_mfma_f32_16x16x32_bf16 v[72:75], v[152:155], v[176:179], v[72:75]
	s_nop 0
	v_mfma_f32_16x16x32_bf16 v[72:75], v[156:159], v[180:183], v[72:75]
	v_mfma_f32_16x16x32_bf16 v[68:71], v[144:147], v[184:187], v[68:71]
	s_nop 0
	v_mfma_f32_16x16x32_bf16 v[68:71], v[148:151], v[188:191], v[68:71]
	v_mfma_f32_16x16x32_bf16 v[64:67], v[152:155], v[184:187], v[64:67]
	s_nop 0
	v_mfma_f32_16x16x32_bf16 v[64:67], v[156:159], v[188:191], v[64:67]
	s_setprio 0
	s_barrier
	ds_read_b128 v[160:163], v197 offset:16384
	ds_read_b128 v[164:167], v197 offset:17408
	ds_read_b128 v[168:171], v197 offset:18432
	ds_read_b128 v[172:175], v197 offset:19456
	ds_read_b128 v[176:179], v197 offset:20480
	ds_read_b128 v[180:183], v197 offset:21504
	ds_read_b128 v[184:187], v197 offset:22528
	ds_read_b128 v[188:191], v197 offset:23552
	s_mov_b32 m0, s62
	s_add_i32 s91, s90, 0x20000
	buffer_load_dwordx4 v192, s[8:11], s90 offen lds
	s_mov_b32 m0, s63
	s_nop 0
	buffer_load_dwordx4 v192, s[8:11], s91 offen lds
	s_add_i32 s91, s90, 0x2000
	s_mov_b32 m0, s64
	s_nop 0
	buffer_load_dwordx4 v192, s[8:11], s91 offen lds
	s_add_i32 s91, s90, 0x22000
	s_mov_b32 m0, s65
	s_nop 0
	buffer_load_dwordx4 v192, s[8:11], s91 offen lds
	s_mov_b32 m0, s47
	s_add_i32 s91, s66, 0x10000
	buffer_load_dwordx4 v196, s[4:7], s66 offen lds
	s_mov_b32 m0, s68
	s_nop 0
	buffer_load_dwordx4 v196, s[4:7], s91 offen lds
	s_waitcnt vmcnt(8)
	s_waitcnt lgkmcnt(6)
	s_barrier
	s_setprio 1
	v_mfma_f32_16x16x32_bf16 v[60:63], v[128:131], v[160:163], v[60:63]
	v_mfma_f32_16x16x32_bf16 v[60:63], v[132:135], v[164:167], v[60:63]
	v_mfma_f32_16x16x32_bf16 v[56:59], v[136:139], v[160:163], v[56:59]
	s_nop 0
	v_mfma_f32_16x16x32_bf16 v[56:59], v[140:143], v[164:167], v[56:59]
	s_waitcnt lgkmcnt(5)
	v_mfma_f32_16x16x32_bf16 v[52:55], v[128:131], v[168:171], v[52:55]
	s_waitcnt lgkmcnt(4)
	v_mfma_f32_16x16x32_bf16 v[52:55], v[132:135], v[172:175], v[52:55]
	v_mfma_f32_16x16x32_bf16 v[48:51], v[136:139], v[168:171], v[48:51]
	s_nop 0
	v_mfma_f32_16x16x32_bf16 v[48:51], v[140:143], v[172:175], v[48:51]
	s_waitcnt lgkmcnt(3)
	v_mfma_f32_16x16x32_bf16 v[44:47], v[128:131], v[176:179], v[44:47]
	s_waitcnt lgkmcnt(2)
	v_mfma_f32_16x16x32_bf16 v[44:47], v[132:135], v[180:183], v[44:47]
	v_mfma_f32_16x16x32_bf16 v[40:43], v[136:139], v[176:179], v[40:43]
	s_nop 0
	v_mfma_f32_16x16x32_bf16 v[40:43], v[140:143], v[180:183], v[40:43]
	s_waitcnt lgkmcnt(1)
	v_mfma_f32_16x16x32_bf16 v[36:39], v[128:131], v[184:187], v[36:39]
	s_waitcnt lgkmcnt(0)
	v_mfma_f32_16x16x32_bf16 v[36:39], v[132:135], v[188:191], v[36:39]
	v_mfma_f32_16x16x32_bf16 v[32:35], v[136:139], v[184:187], v[32:35]
	s_nop 0
	v_mfma_f32_16x16x32_bf16 v[32:35], v[140:143], v[188:191], v[32:35]
	s_setprio 0
	s_setprio 1
	v_mfma_f32_16x16x32_bf16 v[28:31], v[144:147], v[160:163], v[28:31]
	s_nop 0
	v_mfma_f32_16x16x32_bf16 v[28:31], v[148:151], v[164:167], v[28:31]
	v_mfma_f32_16x16x32_bf16 v[24:27], v[152:155], v[160:163], v[24:27]
	s_nop 0
	v_mfma_f32_16x16x32_bf16 v[24:27], v[156:159], v[164:167], v[24:27]
	v_mfma_f32_16x16x32_bf16 v[20:23], v[144:147], v[168:171], v[20:23]
	s_nop 0
	v_mfma_f32_16x16x32_bf16 v[20:23], v[148:151], v[172:175], v[20:23]
	v_mfma_f32_16x16x32_bf16 v[16:19], v[152:155], v[168:171], v[16:19]
	s_nop 0
	v_mfma_f32_16x16x32_bf16 v[16:19], v[156:159], v[172:175], v[16:19]
	v_mfma_f32_16x16x32_bf16 v[12:15], v[144:147], v[176:179], v[12:15]
	s_nop 0
	v_mfma_f32_16x16x32_bf16 v[12:15], v[148:151], v[180:183], v[12:15]
	v_mfma_f32_16x16x32_bf16 v[8:11], v[152:155], v[176:179], v[8:11]
	s_nop 0
	v_mfma_f32_16x16x32_bf16 v[8:11], v[156:159], v[180:183], v[8:11]
	v_mfma_f32_16x16x32_bf16 v[4:7], v[144:147], v[184:187], v[4:7]
	s_nop 0
	v_mfma_f32_16x16x32_bf16 v[4:7], v[148:151], v[188:191], v[4:7]
	v_mfma_f32_16x16x32_bf16 v[0:3], v[152:155], v[184:187], v[0:3]
	s_nop 0
	v_mfma_f32_16x16x32_bf16 v[0:3], v[156:159], v[188:191], v[0:3]
	s_setprio 0
	s_barrier
	ds_read_b128 v[140:143], v203
	ds_read_b128 v[144:147], v204
	ds_read_b128 v[148:151], v205
	ds_read_b128 v[152:155], v206
	ds_read_b128 v[156:159], v207
	ds_read_b128 v[136:139], v208
	ds_read_b128 v[132:135], v209
	ds_read_b128 v[128:131], v210
	ds_read_b128 v[160:163], v197 offset:32768
	ds_read_b128 v[164:167], v197 offset:33792
	ds_read_b128 v[168:171], v197 offset:34816
	ds_read_b128 v[172:175], v197 offset:35840
	ds_read_b128 v[176:179], v197 offset:36864
	ds_read_b128 v[180:183], v197 offset:37888
	ds_read_b128 v[184:187], v197 offset:38912
	ds_read_b128 v[188:191], v197 offset:39936
	s_mov_b32 m0, s69
	s_add_i32 s91, s66, 0x20000
	buffer_load_dwordx4 v196, s[4:7], s91 offen lds
	s_add_i32 s91, s66, 0x30000
	s_mov_b32 m0, s70
	s_nop 0
	buffer_load_dwordx4 v196, s[4:7], s91 offen lds
	s_waitcnt vmcnt(8)
	s_waitcnt lgkmcnt(8)
	s_barrier
	s_setprio 1
	s_waitcnt lgkmcnt(7)
	v_mfma_f32_16x16x32_bf16 v[124:127], v[140:143], v[160:163], v[124:127]
	s_waitcnt lgkmcnt(6)
	v_mfma_f32_16x16x32_bf16 v[124:127], v[144:147], v[164:167], v[124:127]
	v_mfma_f32_16x16x32_bf16 v[120:123], v[148:151], v[160:163], v[120:123]
	s_nop 0
	v_mfma_f32_16x16x32_bf16 v[120:123], v[152:155], v[164:167], v[120:123]
	s_waitcnt lgkmcnt(5)
	v_mfma_f32_16x16x32_bf16 v[116:119], v[140:143], v[168:171], v[116:119]
	s_waitcnt lgkmcnt(4)
	v_mfma_f32_16x16x32_bf16 v[116:119], v[144:147], v[172:175], v[116:119]
	v_mfma_f32_16x16x32_bf16 v[112:115], v[148:151], v[168:171], v[112:115]
	s_nop 0
	v_mfma_f32_16x16x32_bf16 v[112:115], v[152:155], v[172:175], v[112:115]
	s_waitcnt lgkmcnt(3)
	v_mfma_f32_16x16x32_bf16 v[108:111], v[140:143], v[176:179], v[108:111]
	s_waitcnt lgkmcnt(2)
	v_mfma_f32_16x16x32_bf16 v[108:111], v[144:147], v[180:183], v[108:111]
	v_mfma_f32_16x16x32_bf16 v[104:107], v[148:151], v[176:179], v[104:107]
	s_nop 0
	v_mfma_f32_16x16x32_bf16 v[104:107], v[152:155], v[180:183], v[104:107]
	s_waitcnt lgkmcnt(1)
	v_mfma_f32_16x16x32_bf16 v[100:103], v[140:143], v[184:187], v[100:103]
	s_waitcnt lgkmcnt(0)
	v_mfma_f32_16x16x32_bf16 v[100:103], v[144:147], v[188:191], v[100:103]
	v_mfma_f32_16x16x32_bf16 v[96:99], v[148:151], v[184:187], v[96:99]
	s_nop 0
	v_mfma_f32_16x16x32_bf16 v[96:99], v[152:155], v[188:191], v[96:99]
	s_setprio 0
	s_setprio 1
	v_mfma_f32_16x16x32_bf16 v[92:95], v[156:159], v[160:163], v[92:95]
	s_nop 0
	v_mfma_f32_16x16x32_bf16 v[92:95], v[136:139], v[164:167], v[92:95]
	v_mfma_f32_16x16x32_bf16 v[88:91], v[132:135], v[160:163], v[88:91]
	s_nop 0
	v_mfma_f32_16x16x32_bf16 v[88:91], v[128:131], v[164:167], v[88:91]
	v_mfma_f32_16x16x32_bf16 v[84:87], v[156:159], v[168:171], v[84:87]
	s_nop 0
	v_mfma_f32_16x16x32_bf16 v[84:87], v[136:139], v[172:175], v[84:87]
	v_mfma_f32_16x16x32_bf16 v[80:83], v[132:135], v[168:171], v[80:83]
	s_nop 0
	v_mfma_f32_16x16x32_bf16 v[80:83], v[128:131], v[172:175], v[80:83]
	v_mfma_f32_16x16x32_bf16 v[76:79], v[156:159], v[176:179], v[76:79]
	s_nop 0
	v_mfma_f32_16x16x32_bf16 v[76:79], v[136:139], v[180:183], v[76:79]
	v_mfma_f32_16x16x32_bf16 v[72:75], v[132:135], v[176:179], v[72:75]
	s_nop 0
	v_mfma_f32_16x16x32_bf16 v[72:75], v[128:131], v[180:183], v[72:75]
	v_mfma_f32_16x16x32_bf16 v[68:71], v[156:159], v[184:187], v[68:71]
	s_nop 0
	v_mfma_f32_16x16x32_bf16 v[68:71], v[136:139], v[188:191], v[68:71]
	v_mfma_f32_16x16x32_bf16 v[64:67], v[132:135], v[184:187], v[64:67]
	s_nop 0
	v_mfma_f32_16x16x32_bf16 v[64:67], v[128:131], v[188:191], v[64:67]
	s_setprio 0
	s_barrier
	ds_read_b128 v[160:163], v197 offset:49152
	ds_read_b128 v[164:167], v197 offset:50176
	ds_read_b128 v[168:171], v197 offset:51200
	ds_read_b128 v[172:175], v197 offset:52224
	ds_read_b128 v[176:179], v197 offset:53248
	ds_read_b128 v[180:183], v197 offset:54272
	ds_read_b128 v[184:187], v197 offset:55296
	ds_read_b128 v[188:191], v197 offset:56320
	s_mov_b32 m0, s72
	s_add_i32 s91, s90, 0x80
	buffer_load_dwordx4 v192, s[8:11], s91 offen lds
	s_add_i32 s91, s90, 0x20080
	s_mov_b32 m0, s73
	s_add_i32 s66, s66, 0x10080
	buffer_load_dwordx4 v192, s[8:11], s91 offen lds
	s_add_i32 s91, s90, 0x2080
	s_mov_b32 m0, s76
	s_add_i32 s90, s90, 0x22080
	buffer_load_dwordx4 v192, s[8:11], s91 offen lds
	s_mov_b32 m0, s77
	s_nop 0
	buffer_load_dwordx4 v192, s[8:11], s90 offen lds
	s_mov_b32 m0, s74
	s_nop 0
	buffer_load_dwordx4 v196, s[4:7], s67 offen lds
	s_mov_b32 m0, s75
	s_nop 0
	buffer_load_dwordx4 v196, s[4:7], s66 offen lds
	s_waitcnt vmcnt(8)
	s_waitcnt lgkmcnt(6)
	s_barrier
	s_setprio 1
	v_mfma_f32_16x16x32_bf16 v[60:63], v[140:143], v[160:163], v[60:63]
	v_mfma_f32_16x16x32_bf16 v[60:63], v[144:147], v[164:167], v[60:63]
	v_mfma_f32_16x16x32_bf16 v[56:59], v[148:151], v[160:163], v[56:59]
	s_nop 0
	v_mfma_f32_16x16x32_bf16 v[56:59], v[152:155], v[164:167], v[56:59]
	s_waitcnt lgkmcnt(5)
	v_mfma_f32_16x16x32_bf16 v[52:55], v[140:143], v[168:171], v[52:55]
	s_waitcnt lgkmcnt(4)
	v_mfma_f32_16x16x32_bf16 v[52:55], v[144:147], v[172:175], v[52:55]
	v_mfma_f32_16x16x32_bf16 v[48:51], v[148:151], v[168:171], v[48:51]
	s_nop 0
	v_mfma_f32_16x16x32_bf16 v[48:51], v[152:155], v[172:175], v[48:51]
	s_waitcnt lgkmcnt(3)
	v_mfma_f32_16x16x32_bf16 v[44:47], v[140:143], v[176:179], v[44:47]
	s_waitcnt lgkmcnt(2)
	v_mfma_f32_16x16x32_bf16 v[44:47], v[144:147], v[180:183], v[44:47]
	v_mfma_f32_16x16x32_bf16 v[40:43], v[148:151], v[176:179], v[40:43]
	s_nop 0
	v_mfma_f32_16x16x32_bf16 v[40:43], v[152:155], v[180:183], v[40:43]
	s_waitcnt lgkmcnt(1)
	v_mfma_f32_16x16x32_bf16 v[36:39], v[140:143], v[184:187], v[36:39]
	s_waitcnt lgkmcnt(0)
	v_mfma_f32_16x16x32_bf16 v[36:39], v[144:147], v[188:191], v[36:39]
	v_mfma_f32_16x16x32_bf16 v[32:35], v[148:151], v[184:187], v[32:35]
	s_nop 0
	v_mfma_f32_16x16x32_bf16 v[32:35], v[152:155], v[188:191], v[32:35]
	s_setprio 0
	s_setprio 1
	v_mfma_f32_16x16x32_bf16 v[28:31], v[156:159], v[160:163], v[28:31]
	s_nop 0
	v_mfma_f32_16x16x32_bf16 v[28:31], v[136:139], v[164:167], v[28:31]
	v_mfma_f32_16x16x32_bf16 v[24:27], v[132:135], v[160:163], v[24:27]
	s_nop 0
	v_mfma_f32_16x16x32_bf16 v[24:27], v[128:131], v[164:167], v[24:27]
	v_mfma_f32_16x16x32_bf16 v[20:23], v[156:159], v[168:171], v[20:23]
	s_nop 0
	v_mfma_f32_16x16x32_bf16 v[20:23], v[136:139], v[172:175], v[20:23]
	v_mfma_f32_16x16x32_bf16 v[16:19], v[132:135], v[168:171], v[16:19]
	s_nop 0
	v_mfma_f32_16x16x32_bf16 v[16:19], v[128:131], v[172:175], v[16:19]
	v_mfma_f32_16x16x32_bf16 v[12:15], v[156:159], v[176:179], v[12:15]
	s_nop 0
	v_mfma_f32_16x16x32_bf16 v[12:15], v[136:139], v[180:183], v[12:15]
	v_mfma_f32_16x16x32_bf16 v[8:11], v[132:135], v[176:179], v[8:11]
	s_nop 0
	v_mfma_f32_16x16x32_bf16 v[8:11], v[128:131], v[180:183], v[8:11]
	v_mfma_f32_16x16x32_bf16 v[4:7], v[156:159], v[184:187], v[4:7]
	s_nop 0
	v_mfma_f32_16x16x32_bf16 v[4:7], v[136:139], v[188:191], v[4:7]
	v_mfma_f32_16x16x32_bf16 v[0:3], v[132:135], v[184:187], v[0:3]
	s_nop 0
	v_mfma_f32_16x16x32_bf16 v[0:3], v[128:131], v[188:191], v[0:3]
	s_setprio 0
	s_barrier
	s_add_i32 s43, s43, 2
	s_addk_i32 s33, 0x100
	s_addk_i32 s42, 0x100
	s_cmp_gt_u32 s43, 5
	s_cbranch_scc0 .LBB0_254
	s_and_b64 vcc, exec, s[14:15]
	s_cbranch_vccz .LBB0_257
	s_barrier

.LBB0_344:
	s_waitcnt lgkmcnt(0)
	s_add_i32 s4, s60, 0x180
	s_add_i32 s5, s36, 0x180
	s_barrier
	s_setprio 1
	s_waitcnt lgkmcnt(7)
	v_mfma_f32_16x16x32_bf16 v[60:63], v[164:167], v[196:199], 0
	s_waitcnt lgkmcnt(6)
	v_mfma_f32_16x16x32_bf16 v[60:63], v[160:163], v[192:195], v[60:63]
	v_mfma_f32_16x16x32_bf16 v[56:59], v[156:159], v[196:199], 0
	s_nop 0
	v_mfma_f32_16x16x32_bf16 v[56:59], v[152:155], v[192:195], v[56:59]
	s_waitcnt lgkmcnt(5)
	v_mfma_f32_16x16x32_bf16 v[52:55], v[164:167], v[188:191], 0
	s_waitcnt lgkmcnt(4)
	v_mfma_f32_16x16x32_bf16 v[52:55], v[160:163], v[184:187], v[52:55]
	v_mfma_f32_16x16x32_bf16 v[48:51], v[156:159], v[188:191], 0
	s_nop 0
	v_mfma_f32_16x16x32_bf16 v[48:51], v[152:155], v[184:187], v[48:51]
	s_waitcnt lgkmcnt(3)
	v_mfma_f32_16x16x32_bf16 v[44:47], v[164:167], v[180:183], 0
	s_waitcnt lgkmcnt(2)
	v_mfma_f32_16x16x32_bf16 v[44:47], v[160:163], v[176:179], v[44:47]
	v_mfma_f32_16x16x32_bf16 v[40:43], v[156:159], v[180:183], 0
	s_nop 0
	v_mfma_f32_16x16x32_bf16 v[40:43], v[152:155], v[176:179], v[40:43]
	s_waitcnt lgkmcnt(1)
	v_mfma_f32_16x16x32_bf16 v[36:39], v[164:167], v[172:175], 0
	s_waitcnt lgkmcnt(0)
	v_mfma_f32_16x16x32_bf16 v[36:39], v[160:163], v[168:171], v[36:39]
	v_mfma_f32_16x16x32_bf16 v[32:35], v[156:159], v[172:175], 0
	s_nop 0
	v_mfma_f32_16x16x32_bf16 v[32:35], v[152:155], v[168:171], v[32:35]
	s_setprio 0
	s_setprio 1
	v_mfma_f32_16x16x32_bf16 v[28:31], v[148:151], v[196:199], 0
	s_nop 0
	v_mfma_f32_16x16x32_bf16 v[28:31], v[144:147], v[192:195], v[28:31]
	v_mfma_f32_16x16x32_bf16 v[24:27], v[140:143], v[196:199], 0
	s_nop 0
	v_mfma_f32_16x16x32_bf16 v[24:27], v[136:139], v[192:195], v[24:27]
	v_mfma_f32_16x16x32_bf16 v[20:23], v[148:151], v[188:191], 0
	s_nop 0
	v_mfma_f32_16x16x32_bf16 v[20:23], v[144:147], v[184:187], v[20:23]
	v_mfma_f32_16x16x32_bf16 v[16:19], v[140:143], v[188:191], 0
	s_nop 0
	v_mfma_f32_16x16x32_bf16 v[16:19], v[136:139], v[184:187], v[16:19]
	v_mfma_f32_16x16x32_bf16 v[12:15], v[148:151], v[180:183], 0
	s_nop 0
	v_mfma_f32_16x16x32_bf16 v[12:15], v[144:147], v[176:179], v[12:15]
	v_mfma_f32_16x16x32_bf16 v[8:11], v[140:143], v[180:183], 0
	s_nop 0
	v_mfma_f32_16x16x32_bf16 v[8:11], v[136:139], v[176:179], v[8:11]
	v_mfma_f32_16x16x32_bf16 v[4:7], v[148:151], v[172:175], 0
	s_nop 0
	v_mfma_f32_16x16x32_bf16 v[4:7], v[144:147], v[168:171], v[4:7]
	v_mfma_f32_16x16x32_bf16 v[0:3], v[140:143], v[172:175], 0
	s_nop 0
	v_mfma_f32_16x16x32_bf16 v[0:3], v[136:139], v[168:171], v[0:3]
	s_setprio 0
	s_barrier
	ds_read_b128 v[164:167], v225
	ds_read_b128 v[160:163], v226
	ds_read_b128 v[156:159], v227
	ds_read_b128 v[152:155], v228
	ds_read_b128 v[148:151], v229
	ds_read_b128 v[144:147], v230
	ds_read_b128 v[140:143], v231
	ds_read_b128 v[136:139], v232
	ds_read_b128 v[168:171], v233 offset:32768
	ds_read_b128 v[172:175], v233 offset:33792
	ds_read_b128 v[176:179], v233 offset:34816
	ds_read_b128 v[180:183], v233 offset:35840
	ds_read_b128 v[184:187], v233 offset:36864
	ds_read_b128 v[188:191], v233 offset:37888
	ds_read_b128 v[192:195], v233 offset:38912
	ds_read_b128 v[196:199], v233 offset:39936
	s_mov_b32 m0, s72
	s_add_i32 s14, s60, 0x100100
	buffer_load_dwordx4 v214, s[8:11], s14 offen lds
	s_add_i32 s14, s60, 0x180100
	s_mov_b32 m0, s73
	s_nop 0
	buffer_load_dwordx4 v214, s[8:11], s14 offen lds
	s_waitcnt vmcnt(10)
	s_waitcnt lgkmcnt(8)
	s_barrier
	s_setprio 1
	s_waitcnt lgkmcnt(7)
	v_mfma_f32_16x16x32_bf16 v[124:127], v[164:167], v[168:171], v[124:127]
	s_waitcnt lgkmcnt(6)
	v_mfma_f32_16x16x32_bf16 v[124:127], v[160:163], v[172:175], v[124:127]
	v_mfma_f32_16x16x32_bf16 v[120:123], v[156:159], v[168:171], v[120:123]
	s_nop 0
	v_mfma_f32_16x16x32_bf16 v[120:123], v[152:155], v[172:175], v[120:123]
	s_waitcnt lgkmcnt(5)
	v_mfma_f32_16x16x32_bf16 v[116:119], v[164:167], v[176:179], v[116:119]
	s_waitcnt lgkmcnt(4)
	v_mfma_f32_16x16x32_bf16 v[116:119], v[160:163], v[180:183], v[116:119]
	v_mfma_f32_16x16x32_bf16 v[112:115], v[156:159], v[176:179], v[112:115]
	s_nop 0
	v_mfma_f32_16x16x32_bf16 v[112:115], v[152:155], v[180:183], v[112:115]
	s_waitcnt lgkmcnt(3)
	v_mfma_f32_16x16x32_bf16 v[108:111], v[164:167], v[184:187], v[108:111]
	s_waitcnt lgkmcnt(2)
	v_mfma_f32_16x16x32_bf16 v[108:111], v[160:163], v[188:191], v[108:111]
	v_mfma_f32_16x16x32_bf16 v[104:107], v[156:159], v[184:187], v[104:107]
	s_nop 0
	v_mfma_f32_16x16x32_bf16 v[104:107], v[152:155], v[188:191], v[104:107]
	s_waitcnt lgkmcnt(1)
	v_mfma_f32_16x16x32_bf16 v[100:103], v[164:167], v[192:195], v[100:103]
	s_waitcnt lgkmcnt(0)
	v_mfma_f32_16x16x32_bf16 v[100:103], v[160:163], v[196:199], v[100:103]
	v_mfma_f32_16x16x32_bf16 v[96:99], v[156:159], v[192:195], v[96:99]
	s_nop 0
	v_mfma_f32_16x16x32_bf16 v[96:99], v[152:155], v[196:199], v[96:99]
	s_setprio 0
	s_setprio 1
	v_mfma_f32_16x16x32_bf16 v[92:95], v[148:151], v[168:171], v[92:95]
	s_nop 0
	v_mfma_f32_16x16x32_bf16 v[92:95], v[144:147], v[172:175], v[92:95]
	v_mfma_f32_16x16x32_bf16 v[88:91], v[140:143], v[168:171], v[88:91]
	s_nop 0
	v_mfma_f32_16x16x32_bf16 v[88:91], v[136:139], v[172:175], v[88:91]
	v_mfma_f32_16x16x32_bf16 v[84:87], v[148:151], v[176:179], v[84:87]
	s_nop 0
	v_mfma_f32_16x16x32_bf16 v[84:87], v[144:147], v[180:183], v[84:87]
	v_mfma_f32_16x16x32_bf16 v[80:83], v[140:143], v[176:179], v[80:83]
	s_nop 0
	v_mfma_f32_16x16x32_bf16 v[80:83], v[136:139], v[180:183], v[80:83]
	v_mfma_f32_16x16x32_bf16 v[76:79], v[148:151], v[184:187], v[76:79]
	s_nop 0
	v_mfma_f32_16x16x32_bf16 v[76:79], v[144:147], v[188:191], v[76:79]
	v_mfma_f32_16x16x32_bf16 v[72:75], v[140:143], v[184:187], v[72:75]
	s_nop 0
	v_mfma_f32_16x16x32_bf16 v[72:75], v[136:139], v[188:191], v[72:75]
	v_mfma_f32_16x16x32_bf16 v[68:71], v[148:151], v[192:195], v[68:71]
	s_nop 0
	v_mfma_f32_16x16x32_bf16 v[68:71], v[144:147], v[196:199], v[68:71]
	v_mfma_f32_16x16x32_bf16 v[64:67], v[140:143], v[192:195], v[64:67]
	s_nop 0
	v_mfma_f32_16x16x32_bf16 v[64:67], v[136:139], v[196:199], v[64:67]
	s_setprio 0
	s_barrier
	ds_read_b128 v[168:171], v233 offset:49152
	ds_read_b128 v[172:175], v233 offset:50176
	ds_read_b128 v[176:179], v233 offset:51200
	ds_read_b128 v[180:183], v233 offset:52224
	ds_read_b128 v[184:187], v233 offset:53248
	ds_read_b128 v[188:191], v233 offset:54272
	ds_read_b128 v[192:195], v233 offset:55296
	ds_read_b128 v[196:199], v233 offset:56320
	s_mov_b32 m0, s76
	s_mov_b32 s14, s10
	s_mov_b32 s15, s11
	buffer_load_dwordx4 v215, s[12:15], s5 offen lds
	s_add_i32 s5, s36, 0x100180
	s_mov_b32 m0, s77
	s_nop 0
	buffer_load_dwordx4 v215, s[12:15], s5 offen lds
	s_add_i32 s5, s36, 0x10180
	s_mov_b32 m0, s80
	s_nop 0
	buffer_load_dwordx4 v215, s[12:15], s5 offen lds
	s_add_i32 s5, s36, 0x110180
	s_mov_b32 m0, s81
	s_nop 0
	buffer_load_dwordx4 v215, s[12:15], s5 offen lds
	s_mov_b32 m0, s78
	s_nop 0
	buffer_load_dwordx4 v214, s[8:11], s4 offen lds
	s_add_i32 s4, s60, 0x80180
	s_mov_b32 m0, s79
	s_nop 0
	buffer_load_dwordx4 v214, s[8:11], s4 offen lds
	s_waitcnt vmcnt(8)
	s_waitcnt lgkmcnt(6)
	s_barrier
	s_setprio 1
	v_mfma_f32_16x16x32_bf16 v[60:63], v[164:167], v[168:171], v[60:63]
	v_mfma_f32_16x16x32_bf16 v[60:63], v[160:163], v[172:175], v[60:63]
	v_mfma_f32_16x16x32_bf16 v[56:59], v[156:159], v[168:171], v[56:59]
	s_nop 0
	v_mfma_f32_16x16x32_bf16 v[56:59], v[152:155], v[172:175], v[56:59]
	s_waitcnt lgkmcnt(5)
	v_mfma_f32_16x16x32_bf16 v[52:55], v[164:167], v[176:179], v[52:55]
	s_waitcnt lgkmcnt(4)
	v_mfma_f32_16x16x32_bf16 v[52:55], v[160:163], v[180:183], v[52:55]
	v_mfma_f32_16x16x32_bf16 v[48:51], v[156:159], v[176:179], v[48:51]
	s_nop 0
	v_mfma_f32_16x16x32_bf16 v[48:51], v[152:155], v[180:183], v[48:51]
	s_waitcnt lgkmcnt(3)
	v_mfma_f32_16x16x32_bf16 v[44:47], v[164:167], v[184:187], v[44:47]
	s_waitcnt lgkmcnt(2)
	v_mfma_f32_16x16x32_bf16 v[44:47], v[160:163], v[188:191], v[44:47]
	v_mfma_f32_16x16x32_bf16 v[40:43], v[156:159], v[184:187], v[40:43]
	s_nop 0
	v_mfma_f32_16x16x32_bf16 v[40:43], v[152:155], v[188:191], v[40:43]
	s_waitcnt lgkmcnt(1)
	v_mfma_f32_16x16x32_bf16 v[36:39], v[164:167], v[192:195], v[36:39]
	s_waitcnt lgkmcnt(0)
	v_mfma_f32_16x16x32_bf16 v[36:39], v[160:163], v[196:199], v[36:39]
	v_mfma_f32_16x16x32_bf16 v[32:35], v[156:159], v[192:195], v[32:35]
	s_nop 0
	v_mfma_f32_16x16x32_bf16 v[32:35], v[152:155], v[196:199], v[32:35]
	s_setprio 0
	s_setprio 1
	v_mfma_f32_16x16x32_bf16 v[28:31], v[148:151], v[168:171], v[28:31]
	s_nop 0
	v_mfma_f32_16x16x32_bf16 v[28:31], v[144:147], v[172:175], v[28:31]
	v_mfma_f32_16x16x32_bf16 v[24:27], v[140:143], v[168:171], v[24:27]
	s_nop 0
	v_mfma_f32_16x16x32_bf16 v[24:27], v[136:139], v[172:175], v[24:27]
	v_mfma_f32_16x16x32_bf16 v[20:23], v[148:151], v[176:179], v[20:23]
	s_nop 0
	v_mfma_f32_16x16x32_bf16 v[20:23], v[144:147], v[180:183], v[20:23]
	v_mfma_f32_16x16x32_bf16 v[16:19], v[140:143], v[176:179], v[16:19]
	s_nop 0
	v_mfma_f32_16x16x32_bf16 v[16:19], v[136:139], v[180:183], v[16:19]
	v_mfma_f32_16x16x32_bf16 v[12:15], v[148:151], v[184:187], v[12:15]
	s_nop 0
	v_mfma_f32_16x16x32_bf16 v[12:15], v[144:147], v[188:191], v[12:15]
	v_mfma_f32_16x16x32_bf16 v[8:11], v[140:143], v[184:187], v[8:11]
	s_nop 0
	v_mfma_f32_16x16x32_bf16 v[8:11], v[136:139], v[188:191], v[8:11]
	v_mfma_f32_16x16x32_bf16 v[4:7], v[148:151], v[192:195], v[4:7]
	s_nop 0
	v_mfma_f32_16x16x32_bf16 v[4:7], v[144:147], v[196:199], v[4:7]
	v_mfma_f32_16x16x32_bf16 v[0:3], v[140:143], v[192:195], v[0:3]
	s_nop 0
	v_mfma_f32_16x16x32_bf16 v[0:3], v[136:139], v[196:199], v[0:3]
	s_setprio 0
	s_barrier
	s_waitcnt vmcnt(14)
	v_mul_f32_e32 v132, 0x42800000, v132
	v_mul_f32_e32 v128, 0x42800000, v128
	v_mul_f32_e32 v133, 0x42800000, v133
	v_mul_f32_e32 v129, 0x42800000, v129
	v_mul_f32_e32 v134, 0x42800000, v134
	v_mul_f32_e32 v130, 0x42800000, v130
	v_mul_f32_e32 v135, 0x42800000, v135
	v_mul_f32_e32 v131, 0x42800000, v131
	v_cvt_pk_fp8_f32 v204, v128, v132
	v_cvt_pk_fp8_f32 v234, v129, v133
	v_cvt_pk_fp8_f32 v235, v130, v134
	v_cvt_pk_fp8_f32 v236, v131, v135
	s_add_i32 s33, s36, 0x200
	s_mov_b32 s61, 0
	s_mov_b32 s66, s75
	s_mov_b32 s94, s86
	s_branch .LBB0_347

.Lp2_top:
	ds_read_b128 v[158:161], v217
	ds_read_b128 v[162:165], v218
	ds_read_b128 v[166:169], v219
	ds_read_b128 v[170:173], v220
	ds_read_b128 v[148:151], v221
	ds_read_b128 v[144:147], v222
	ds_read_b128 v[140:143], v223
	ds_read_b128 v[136:139], v224
	ds_read_b128 v[174:177], v233
	ds_read_b128 v[178:181], v233 offset:1024
	ds_read_b128 v[182:185], v233 offset:2048
	ds_read_b128 v[186:189], v233 offset:3072
	ds_read_b128 v[190:193], v233 offset:4096
	ds_read_b128 v[194:197], v233 offset:5120
	ds_read_b128 v[234:237], v233 offset:6144
	ds_read_b128 v[238:241], v233 offset:7168
	s_add_i32 s4, s60, s61
	s_mov_b32 s46, s94
	s_add_i32 s94, s94, 1
	s_add_i32 s5, s4, 0x200
	s_add_i32 s16, s33, s61
	s_cmpk_eq_i32 s61, 0x1e00
	s_cselect_b32 s47, s90, s5
	s_cselect_b32 s97, s91, s16
	s_add_i32 s96, s47, 0x80
	s_mov_b32 m0, s82
	s_add_i32 s5, s4, 0x100180
	buffer_load_dwordx4 v214, s[8:11], s5 offen lds
	s_add_i32 s4, s4, 0x180180
	s_mov_b32 m0, s85
	s_add_i32 vcc_lo, s97, 0x80
	buffer_load_dwordx4 v214, s[8:11], s4 offen lds
	s_lshr_b32 s4, s94, 2
	s_mul_i32 s5, s4, s34
	s_add_i32 s16, s5, s2
	s_cmp_lt_i32 s4, s3
	s_cselect_b64 s[4:5], -1, 0
	s_and_b64 s[44:45], s[4:5], exec
	s_cselect_b32 s16, s16, 0
	s_bfe_u32 s17, s94, 0x10001
	s_or_b32 s17, s17, s83
	s_bfe_u32 s67, s16, 0x50007
	s_bfe_u32 s36, s16, 0x50002
	s_and_b32 s95, s16, 3
	s_cmpk_gt_i32 s16, 0xfff
	s_cselect_b64 s[44:45], -1, 0
	v_lshl_or_b32 v156, s17, 3, v216
	s_and_b64 s[16:17], s[44:45], exec
	s_cselect_b32 s16, s25, s21
	s_cselect_b32 s17, s24, s20
	s_lshl_b32 vcc_hi, s67, 23
	s_add_u32 s17, s17, vcc_hi
	s_addc_u32 s16, s16, 0
	s_lshl_b32 vcc_hi, s36, 18
	s_add_u32 s17, s17, vcc_hi
	s_addc_u32 vcc_hi, s16, 0
	s_lshl_b32 s16, s95, 9
	s_add_u32 s16, s17, s16
	v_and_or_b32 v204, s66, 2, v200
	s_addc_u32 s17, vcc_hi, 0
	v_lshlrev_b64 v[128:129], 11, v[204:205]
	v_lshl_add_u64 v[128:129], s[16:17], 0, v[128:129]
	v_lshlrev_b32_e32 v204, 4, v156
	v_lshl_add_u64 v[132:133], v[128:129], 0, v[204:205]
	global_load_dwordx4 v[128:131], v[132:133], off nt
	s_nop 0
	global_load_dwordx4 v[132:135], v[132:133], off offset:2048 nt
	s_waitcnt vmcnt(10)
	s_waitcnt lgkmcnt(8)
	s_barrier
	s_setprio 1
	s_waitcnt lgkmcnt(7)
	v_mfma_f32_16x16x32_bf16 v[124:127], v[158:161], v[174:177], v[124:127]
	s_waitcnt lgkmcnt(6)
	v_mfma_f32_16x16x32_bf16 v[124:127], v[162:165], v[178:181], v[124:127]
	v_mfma_f32_16x16x32_bf16 v[120:123], v[166:169], v[174:177], v[120:123]
	s_nop 0
	v_mfma_f32_16x16x32_bf16 v[120:123], v[170:173], v[178:181], v[120:123]
	s_waitcnt lgkmcnt(5)
	v_mfma_f32_16x16x32_bf16 v[116:119], v[158:161], v[182:185], v[116:119]
	s_waitcnt lgkmcnt(4)
	v_mfma_f32_16x16x32_bf16 v[116:119], v[162:165], v[186:189], v[116:119]
	v_mfma_f32_16x16x32_bf16 v[112:115], v[166:169], v[182:185], v[112:115]
	s_nop 0
	v_mfma_f32_16x16x32_bf16 v[112:115], v[170:173], v[186:189], v[112:115]
	s_waitcnt lgkmcnt(3)
	v_mfma_f32_16x16x32_bf16 v[108:111], v[158:161], v[190:193], v[108:111]
	s_waitcnt lgkmcnt(2)
	v_mfma_f32_16x16x32_bf16 v[108:111], v[162:165], v[194:197], v[108:111]
	v_mfma_f32_16x16x32_bf16 v[104:107], v[166:169], v[190:193], v[104:107]
	s_nop 0
	v_mfma_f32_16x16x32_bf16 v[104:107], v[170:173], v[194:197], v[104:107]
	s_waitcnt lgkmcnt(1)
	v_mfma_f32_16x16x32_bf16 v[100:103], v[158:161], v[234:237], v[100:103]
	s_waitcnt lgkmcnt(0)
	v_mfma_f32_16x16x32_bf16 v[100:103], v[162:165], v[238:241], v[100:103]
	v_mfma_f32_16x16x32_bf16 v[96:99], v[166:169], v[234:237], v[96:99]
	s_nop 0
	v_mfma_f32_16x16x32_bf16 v[96:99], v[170:173], v[238:241], v[96:99]
	s_setprio 0
	s_setprio 1
	v_mfma_f32_16x16x32_bf16 v[92:95], v[148:151], v[174:177], v[92:95]
	s_nop 0
	v_mfma_f32_16x16x32_bf16 v[92:95], v[144:147], v[178:181], v[92:95]
	v_mfma_f32_16x16x32_bf16 v[88:91], v[140:143], v[174:177], v[88:91]
	s_nop 0
	v_mfma_f32_16x16x32_bf16 v[88:91], v[136:139], v[178:181], v[88:91]
	v_mfma_f32_16x16x32_bf16 v[84:87], v[148:151], v[182:185], v[84:87]
	s_nop 0
	v_mfma_f32_16x16x32_bf16 v[84:87], v[144:147], v[186:189], v[84:87]
	v_mfma_f32_16x16x32_bf16 v[80:83], v[140:143], v[182:185], v[80:83]
	s_nop 0
	v_mfma_f32_16x16x32_bf16 v[80:83], v[136:139], v[186:189], v[80:83]
	v_mfma_f32_16x16x32_bf16 v[76:79], v[148:151], v[190:193], v[76:79]
	s_nop 0
	v_mfma_f32_16x16x32_bf16 v[76:79], v[144:147], v[194:197], v[76:79]
	v_mfma_f32_16x16x32_bf16 v[72:75], v[140:143], v[190:193], v[72:75]
	s_nop 0
	v_mfma_f32_16x16x32_bf16 v[72:75], v[136:139], v[194:197], v[72:75]
	v_mfma_f32_16x16x32_bf16 v[68:71], v[148:151], v[234:237], v[68:71]
	s_nop 0
	v_mfma_f32_16x16x32_bf16 v[68:71], v[144:147], v[238:241], v[68:71]
	v_mfma_f32_16x16x32_bf16 v[64:67], v[140:143], v[234:237], v[64:67]
	s_nop 0
	v_mfma_f32_16x16x32_bf16 v[64:67], v[136:139], v[238:241], v[64:67]
	s_setprio 0
	s_barrier
	ds_read_b128 v[174:177], v233 offset:16384
	ds_read_b128 v[178:181], v233 offset:17408
	ds_read_b128 v[182:185], v233 offset:18432
	ds_read_b128 v[186:189], v233 offset:19456
	ds_read_b128 v[190:193], v233 offset:20480
	ds_read_b128 v[194:197], v233 offset:21504
	ds_read_b128 v[234:237], v233 offset:22528
	ds_read_b128 v[238:241], v233 offset:23552
	s_mov_b32 m0, s65
	s_add_i32 s16, s97, 0x100000
	buffer_load_dwordx4 v215, s[12:15], s97 offen lds
	s_mov_b32 m0, s68
	s_nop 0
	buffer_load_dwordx4 v215, s[12:15], s16 offen lds
	s_add_i32 s16, s97, 0x10000
	s_mov_b32 m0, s69
	s_nop 0
	buffer_load_dwordx4 v215, s[12:15], s16 offen lds
	s_add_i32 s16, s97, 0x110000
	s_mov_b32 m0, s70
	s_nop 0
	buffer_load_dwordx4 v215, s[12:15], s16 offen lds
	s_mov_b32 m0, s64
	s_add_i32 s16, s47, 0x80000
	buffer_load_dwordx4 v214, s[8:11], s47 offen lds
	s_mov_b32 m0, s71
	s_nop 0
	buffer_load_dwordx4 v214, s[8:11], s16 offen lds
	s_waitcnt vmcnt(10)
	s_waitcnt lgkmcnt(6)
	s_barrier
	s_setprio 1
	v_mfma_f32_16x16x32_bf16 v[60:63], v[158:161], v[174:177], v[60:63]
	v_mfma_f32_16x16x32_bf16 v[60:63], v[162:165], v[178:181], v[60:63]
	v_mfma_f32_16x16x32_bf16 v[56:59], v[166:169], v[174:177], v[56:59]
	s_nop 0
	v_mfma_f32_16x16x32_bf16 v[56:59], v[170:173], v[178:181], v[56:59]
	s_waitcnt lgkmcnt(5)
	v_mfma_f32_16x16x32_bf16 v[52:55], v[158:161], v[182:185], v[52:55]
	s_waitcnt lgkmcnt(4)
	v_mfma_f32_16x16x32_bf16 v[52:55], v[162:165], v[186:189], v[52:55]
	v_mfma_f32_16x16x32_bf16 v[48:51], v[166:169], v[182:185], v[48:51]
	s_nop 0
	v_mfma_f32_16x16x32_bf16 v[48:51], v[170:173], v[186:189], v[48:51]
	s_waitcnt lgkmcnt(3)
	v_mfma_f32_16x16x32_bf16 v[44:47], v[158:161], v[190:193], v[44:47]
	s_waitcnt lgkmcnt(2)
	v_mfma_f32_16x16x32_bf16 v[44:47], v[162:165], v[194:197], v[44:47]
	v_mfma_f32_16x16x32_bf16 v[40:43], v[166:169], v[190:193], v[40:43]
	s_nop 0
	v_mfma_f32_16x16x32_bf16 v[40:43], v[170:173], v[194:197], v[40:43]
	s_waitcnt lgkmcnt(1)
	v_mfma_f32_16x16x32_bf16 v[36:39], v[158:161], v[234:237], v[36:39]
	s_waitcnt lgkmcnt(0)
	v_mfma_f32_16x16x32_bf16 v[36:39], v[162:165], v[238:241], v[36:39]
	v_mfma_f32_16x16x32_bf16 v[32:35], v[166:169], v[234:237], v[32:35]
	s_nop 0
	v_mfma_f32_16x16x32_bf16 v[32:35], v[170:173], v[238:241], v[32:35]
	s_setprio 0
	s_setprio 1
	v_mfma_f32_16x16x32_bf16 v[28:31], v[148:151], v[174:177], v[28:31]
	s_nop 0
	v_mfma_f32_16x16x32_bf16 v[28:31], v[144:147], v[178:181], v[28:31]
	v_mfma_f32_16x16x32_bf16 v[24:27], v[140:143], v[174:177], v[24:27]
	s_nop 0
	v_mfma_f32_16x16x32_bf16 v[24:27], v[136:139], v[178:181], v[24:27]
	v_mfma_f32_16x16x32_bf16 v[20:23], v[148:151], v[182:185], v[20:23]
	s_nop 0
	v_mfma_f32_16x16x32_bf16 v[20:23], v[144:147], v[186:189], v[20:23]
	v_mfma_f32_16x16x32_bf16 v[16:19], v[140:143], v[182:185], v[16:19]
	s_nop 0
	v_mfma_f32_16x16x32_bf16 v[16:19], v[136:139], v[186:189], v[16:19]
	v_mfma_f32_16x16x32_bf16 v[12:15], v[148:151], v[190:193], v[12:15]
	s_nop 0
	v_mfma_f32_16x16x32_bf16 v[12:15], v[144:147], v[194:197], v[12:15]
	v_mfma_f32_16x16x32_bf16 v[8:11], v[140:143], v[190:193], v[8:11]
	s_nop 0
	v_mfma_f32_16x16x32_bf16 v[8:11], v[136:139], v[194:197], v[8:11]
	v_mfma_f32_16x16x32_bf16 v[4:7], v[148:151], v[234:237], v[4:7]
	s_nop 0
	v_mfma_f32_16x16x32_bf16 v[4:7], v[144:147], v[238:241], v[4:7]
	v_mfma_f32_16x16x32_bf16 v[0:3], v[140:143], v[234:237], v[0:3]
	s_nop 0
	v_mfma_f32_16x16x32_bf16 v[0:3], v[136:139], v[238:241], v[0:3]
	s_setprio 0
	s_barrier
	ds_read_b128 v[136:139], v225
	ds_read_b128 v[140:143], v226
	ds_read_b128 v[144:147], v227
	ds_read_b128 v[148:151], v228
	ds_read_b128 v[158:161], v229
	ds_read_b128 v[162:165], v230
	ds_read_b128 v[166:169], v231
	ds_read_b128 v[170:173], v232
	ds_read_b128 v[174:177], v233 offset:32768
	ds_read_b128 v[178:181], v233 offset:33792
	ds_read_b128 v[182:185], v233 offset:34816
	ds_read_b128 v[186:189], v233 offset:35840
	ds_read_b128 v[190:193], v233 offset:36864
	ds_read_b128 v[194:197], v233 offset:37888
	ds_read_b128 v[234:237], v233 offset:38912
	ds_read_b128 v[238:241], v233 offset:39936
	s_mov_b32 m0, s72
	s_add_i32 s16, s47, 0x100000
	buffer_load_dwordx4 v214, s[8:11], s16 offen lds
	s_add_i32 s16, s47, 0x180000
	s_mov_b32 m0, s73
	s_nop 0
	buffer_load_dwordx4 v214, s[8:11], s16 offen lds
	s_waitcnt vmcnt(10)
	s_waitcnt lgkmcnt(8)
	s_barrier
	s_setprio 1
	s_waitcnt lgkmcnt(7)
	v_mfma_f32_16x16x32_bf16 v[124:127], v[136:139], v[174:177], v[124:127]
	s_waitcnt lgkmcnt(6)
	v_mfma_f32_16x16x32_bf16 v[124:127], v[140:143], v[178:181], v[124:127]
	v_mfma_f32_16x16x32_bf16 v[120:123], v[144:147], v[174:177], v[120:123]
	s_nop 0
	v_mfma_f32_16x16x32_bf16 v[120:123], v[148:151], v[178:181], v[120:123]
	s_waitcnt lgkmcnt(5)
	v_mfma_f32_16x16x32_bf16 v[116:119], v[136:139], v[182:185], v[116:119]
	s_waitcnt lgkmcnt(4)
	v_mfma_f32_16x16x32_bf16 v[116:119], v[140:143], v[186:189], v[116:119]
	v_mfma_f32_16x16x32_bf16 v[112:115], v[144:147], v[182:185], v[112:115]
	s_nop 0
	v_mfma_f32_16x16x32_bf16 v[112:115], v[148:151], v[186:189], v[112:115]
	s_waitcnt lgkmcnt(3)
	v_mfma_f32_16x16x32_bf16 v[108:111], v[136:139], v[190:193], v[108:111]
	s_waitcnt lgkmcnt(2)
	v_mfma_f32_16x16x32_bf16 v[108:111], v[140:143], v[194:197], v[108:111]
	v_mfma_f32_16x16x32_bf16 v[104:107], v[144:147], v[190:193], v[104:107]
	s_nop 0
	v_mfma_f32_16x16x32_bf16 v[104:107], v[148:151], v[194:197], v[104:107]
	s_waitcnt lgkmcnt(1)
	v_mfma_f32_16x16x32_bf16 v[100:103], v[136:139], v[234:237], v[100:103]
	s_waitcnt lgkmcnt(0)
	v_mfma_f32_16x16x32_bf16 v[100:103], v[140:143], v[238:241], v[100:103]
	v_mfma_f32_16x16x32_bf16 v[96:99], v[144:147], v[234:237], v[96:99]
	s_nop 0
	v_mfma_f32_16x16x32_bf16 v[96:99], v[148:151], v[238:241], v[96:99]
	s_setprio 0
	s_setprio 1
	v_mfma_f32_16x16x32_bf16 v[92:95], v[158:161], v[174:177], v[92:95]
	s_nop 0
	v_mfma_f32_16x16x32_bf16 v[92:95], v[162:165], v[178:181], v[92:95]
	v_mfma_f32_16x16x32_bf16 v[88:91], v[166:169], v[174:177], v[88:91]
	s_nop 0
	v_mfma_f32_16x16x32_bf16 v[88:91], v[170:173], v[178:181], v[88:91]
	v_mfma_f32_16x16x32_bf16 v[84:87], v[158:161], v[182:185], v[84:87]
	s_nop 0
	v_mfma_f32_16x16x32_bf16 v[84:87], v[162:165], v[186:189], v[84:87]
	v_mfma_f32_16x16x32_bf16 v[80:83], v[166:169], v[182:185], v[80:83]
	s_nop 0
	v_mfma_f32_16x16x32_bf16 v[80:83], v[170:173], v[186:189], v[80:83]
	v_mfma_f32_16x16x32_bf16 v[76:79], v[158:161], v[190:193], v[76:79]
	s_nop 0
	v_mfma_f32_16x16x32_bf16 v[76:79], v[162:165], v[194:197], v[76:79]
	v_mfma_f32_16x16x32_bf16 v[72:75], v[166:169], v[190:193], v[72:75]
	s_nop 0
	v_mfma_f32_16x16x32_bf16 v[72:75], v[170:173], v[194:197], v[72:75]
	v_mfma_f32_16x16x32_bf16 v[68:71], v[158:161], v[234:237], v[68:71]
	s_nop 0
	v_mfma_f32_16x16x32_bf16 v[68:71], v[162:165], v[238:241], v[68:71]
	v_mfma_f32_16x16x32_bf16 v[64:67], v[166:169], v[234:237], v[64:67]
	s_nop 0
	v_mfma_f32_16x16x32_bf16 v[64:67], v[170:173], v[238:241], v[64:67]
	s_setprio 0
	s_barrier
	ds_read_b128 v[174:177], v233 offset:49152
	ds_read_b128 v[178:181], v233 offset:50176
	ds_read_b128 v[182:185], v233 offset:51200
	ds_read_b128 v[186:189], v233 offset:52224
	ds_read_b128 v[190:193], v233 offset:53248
	ds_read_b128 v[194:197], v233 offset:54272
	ds_read_b128 v[234:237], v233 offset:55296
	ds_read_b128 v[238:241], v233 offset:56320
	s_mov_b32 m0, s76
	s_add_i32 s16, s97, 0x100080
	buffer_load_dwordx4 v215, s[12:15], vcc_lo offen lds
	s_mov_b32 m0, s77
	s_add_i32 s47, s47, 0x80080
	buffer_load_dwordx4 v215, s[12:15], s16 offen lds
	s_add_i32 s16, s97, 0x10080
	s_mov_b32 m0, s80
	s_add_i32 s97, s97, 0x110080
	buffer_load_dwordx4 v215, s[12:15], s16 offen lds
	s_mov_b32 m0, s81
	s_nop 0
	buffer_load_dwordx4 v215, s[12:15], s97 offen lds
	s_mov_b32 m0, s78
	s_nop 0
	buffer_load_dwordx4 v214, s[8:11], s96 offen lds
	s_mov_b32 m0, s79
	s_nop 0
	buffer_load_dwordx4 v214, s[8:11], s47 offen lds
	s_bitcmp0_b32 s46, 0
	s_mov_b32 s98, 0xffff
	s_cselect_b32 s98, 0xffff0000, s98
	s_waitcnt vmcnt(8)
	s_waitcnt lgkmcnt(6)
	s_barrier
	s_setprio 1
	v_mfma_f32_16x16x32_bf16 v[60:63], v[136:139], v[174:177], v[60:63]
	v_mfma_f32_16x16x32_bf16 v[60:63], v[140:143], v[178:181], v[60:63]
	v_mfma_f32_16x16x32_bf16 v[56:59], v[144:147], v[174:177], v[56:59]
	v_mul_f32_e32 v128, 0x42800000, v128
	v_mfma_f32_16x16x32_bf16 v[56:59], v[148:151], v[178:181], v[56:59]
	v_mul_f32_e32 v130, 0x42800000, v130
	s_waitcnt lgkmcnt(5)
	v_mfma_f32_16x16x32_bf16 v[52:55], v[136:139], v[182:185], v[52:55]
	s_waitcnt lgkmcnt(4)
	v_mfma_f32_16x16x32_bf16 v[52:55], v[140:143], v[186:189], v[52:55]
	v_mfma_f32_16x16x32_bf16 v[48:51], v[144:147], v[182:185], v[48:51]
	v_mul_f32_e32 v132, 0x42800000, v132
	v_mfma_f32_16x16x32_bf16 v[48:51], v[148:151], v[186:189], v[48:51]
	v_mul_f32_e32 v134, 0x42800000, v134
	s_waitcnt lgkmcnt(3)
	v_mfma_f32_16x16x32_bf16 v[44:47], v[136:139], v[190:193], v[44:47]
	s_waitcnt lgkmcnt(2)
	v_mfma_f32_16x16x32_bf16 v[44:47], v[140:143], v[194:197], v[44:47]
	v_mfma_f32_16x16x32_bf16 v[40:43], v[144:147], v[190:193], v[40:43]
	v_mul_f32_e32 v129, 0x42800000, v129
	v_mfma_f32_16x16x32_bf16 v[40:43], v[148:151], v[194:197], v[40:43]
	v_mul_f32_e32 v131, 0x42800000, v131
	s_waitcnt lgkmcnt(1)
	v_mfma_f32_16x16x32_bf16 v[36:39], v[136:139], v[234:237], v[36:39]
	s_waitcnt lgkmcnt(0)
	v_mfma_f32_16x16x32_bf16 v[36:39], v[140:143], v[238:241], v[36:39]
	v_mfma_f32_16x16x32_bf16 v[32:35], v[144:147], v[234:237], v[32:35]
	v_mul_f32_e32 v133, 0x42800000, v133
	v_mfma_f32_16x16x32_bf16 v[32:35], v[148:151], v[238:241], v[32:35]
	v_mul_f32_e32 v135, 0x42800000, v135
	s_setprio 0
	s_setprio 1
	v_mfma_f32_16x16x32_bf16 v[28:31], v[158:161], v[174:177], v[28:31]
	v_cvt_pk_fp8_f32 v204, v128, v132
	v_mfma_f32_16x16x32_bf16 v[28:31], v[162:165], v[178:181], v[28:31]
	v_mfma_f32_16x16x32_bf16 v[24:27], v[166:169], v[174:177], v[24:27]
	v_cvt_pk_fp8_f32 v204, v128, v132 op_sel:[0,0,1]
	v_mfma_f32_16x16x32_bf16 v[24:27], v[170:173], v[178:181], v[24:27]
	v_mfma_f32_16x16x32_bf16 v[20:23], v[158:161], v[182:185], v[20:23]
	v_cvt_pk_fp8_f32 v250, v129, v133
	v_mfma_f32_16x16x32_bf16 v[20:23], v[162:165], v[186:189], v[20:23]
	v_mfma_f32_16x16x32_bf16 v[16:19], v[166:169], v[182:185], v[16:19]
	v_cvt_pk_fp8_f32 v250, v129, v133 op_sel:[0,0,1]
	v_mfma_f32_16x16x32_bf16 v[16:19], v[170:173], v[186:189], v[16:19]
	v_mfma_f32_16x16x32_bf16 v[12:15], v[158:161], v[190:193], v[12:15]
	v_cvt_pk_fp8_f32 v251, v130, v134
	v_mfma_f32_16x16x32_bf16 v[12:15], v[162:165], v[194:197], v[12:15]
	v_bfi_b32 v152, s98, v204, v152
	v_mfma_f32_16x16x32_bf16 v[8:11], v[166:169], v[190:193], v[8:11]
	v_cvt_pk_fp8_f32 v251, v130, v134 op_sel:[0,0,1]
	v_mfma_f32_16x16x32_bf16 v[8:11], v[170:173], v[194:197], v[8:11]
	v_bfi_b32 v153, s98, v250, v153
	v_mfma_f32_16x16x32_bf16 v[4:7], v[158:161], v[234:237], v[4:7]
	v_cvt_pk_fp8_f32 v252, v131, v135
	v_mfma_f32_16x16x32_bf16 v[4:7], v[162:165], v[238:241], v[4:7]
	v_bfi_b32 v154, s98, v251, v154
	v_mfma_f32_16x16x32_bf16 v[0:3], v[166:169], v[234:237], v[0:3]
	v_cvt_pk_fp8_f32 v252, v131, v135 op_sel:[0,0,1]
	v_mfma_f32_16x16x32_bf16 v[0:3], v[170:173], v[238:241], v[0:3]
	v_bfi_b32 v155, s98, v252, v155
	s_setprio 0
	s_barrier
	s_bitcmp0_b32 s46, 0
	s_mov_b64 s[46:47], -1
	s_cbranch_scc0 .LBB0_345
	s_andn2_b64 vcc, exec, s[4:5]
	s_cbranch_vccnz .LBB0_345
	s_lshl_b32 s4, s67, 10
	s_lshl_b32 s5, s95, 8
	s_or_b32 s16, s4, s5
	s_and_b64 s[4:5], s[44:45], exec
	s_cselect_b32 s4, 8, 0
	v_lshlrev_b32_e32 v128, 3, v156
	s_or_b32 s4, s4, s16
	v_and_b32_e32 v128, 0xf0, v128
	v_or_b32_e32 v128, s4, v128
	v_or_b32_e32 v204, v128, v202
	v_lshlrev_b64 v[128:129], 12, v[204:205]
	v_lshl_add_u64 v[128:129], s[6:7], 0, v[128:129]
	s_lshl_b32 s36, s36, 7
	v_lshl_add_u64 v[128:129], v[128:129], 0, s[36:37]
	v_lshl_add_u64 v[128:129], v[128:129], 0, v[200:201]
	v_add_co_u32_e32 v130, vcc, 0x1000, v128
	global_store_dword v[128:129], v152, off
	s_nop 0
	v_addc_co_u32_e32 v131, vcc, 0, v129, vcc
	global_store_dword v[130:131], v153, off
	v_add_co_u32_e32 v130, vcc, 0x2000, v128
	s_nop 1
	v_addc_co_u32_e32 v131, vcc, 0, v129, vcc
	v_add_co_u32_e32 v128, vcc, 0x3000, v128
	global_store_dword v[130:131], v154, off
	s_nop 0
	v_addc_co_u32_e32 v129, vcc, 0, v129, vcc
	global_store_dword v[128:129], v155, off
	s_branch .LBB0_345

.LBB0_592:
	s_waitcnt lgkmcnt(0)
	s_add_i32 s4, s60, 0x180
	s_add_i32 s5, s42, 0x180
	s_barrier
	s_setprio 1
	s_waitcnt lgkmcnt(7)
	v_mfma_f32_16x16x32_bf16 v[60:63], v[164:167], v[196:199], 0
	s_waitcnt lgkmcnt(6)
	v_mfma_f32_16x16x32_bf16 v[60:63], v[160:163], v[192:195], v[60:63]
	v_mfma_f32_16x16x32_bf16 v[56:59], v[156:159], v[196:199], 0
	s_nop 0
	v_mfma_f32_16x16x32_bf16 v[56:59], v[152:155], v[192:195], v[56:59]
	s_waitcnt lgkmcnt(5)
	v_mfma_f32_16x16x32_bf16 v[52:55], v[164:167], v[188:191], 0
	s_waitcnt lgkmcnt(4)
	v_mfma_f32_16x16x32_bf16 v[52:55], v[160:163], v[184:187], v[52:55]
	v_mfma_f32_16x16x32_bf16 v[48:51], v[156:159], v[188:191], 0
	s_nop 0
	v_mfma_f32_16x16x32_bf16 v[48:51], v[152:155], v[184:187], v[48:51]
	s_waitcnt lgkmcnt(3)
	v_mfma_f32_16x16x32_bf16 v[44:47], v[164:167], v[180:183], 0
	s_waitcnt lgkmcnt(2)
	v_mfma_f32_16x16x32_bf16 v[44:47], v[160:163], v[176:179], v[44:47]
	v_mfma_f32_16x16x32_bf16 v[40:43], v[156:159], v[180:183], 0
	s_nop 0
	v_mfma_f32_16x16x32_bf16 v[40:43], v[152:155], v[176:179], v[40:43]
	s_waitcnt lgkmcnt(1)
	v_mfma_f32_16x16x32_bf16 v[36:39], v[164:167], v[172:175], 0
	s_waitcnt lgkmcnt(0)
	v_mfma_f32_16x16x32_bf16 v[36:39], v[160:163], v[168:171], v[36:39]
	v_mfma_f32_16x16x32_bf16 v[32:35], v[156:159], v[172:175], 0
	s_nop 0
	v_mfma_f32_16x16x32_bf16 v[32:35], v[152:155], v[168:171], v[32:35]
	s_setprio 0
	s_setprio 1
	v_mfma_f32_16x16x32_bf16 v[28:31], v[148:151], v[196:199], 0
	s_nop 0
	v_mfma_f32_16x16x32_bf16 v[28:31], v[144:147], v[192:195], v[28:31]
	v_mfma_f32_16x16x32_bf16 v[24:27], v[140:143], v[196:199], 0
	s_nop 0
	v_mfma_f32_16x16x32_bf16 v[24:27], v[136:139], v[192:195], v[24:27]
	v_mfma_f32_16x16x32_bf16 v[20:23], v[148:151], v[188:191], 0
	s_nop 0
	v_mfma_f32_16x16x32_bf16 v[20:23], v[144:147], v[184:187], v[20:23]
	v_mfma_f32_16x16x32_bf16 v[16:19], v[140:143], v[188:191], 0
	s_nop 0
	v_mfma_f32_16x16x32_bf16 v[16:19], v[136:139], v[184:187], v[16:19]
	v_mfma_f32_16x16x32_bf16 v[12:15], v[148:151], v[180:183], 0
	s_nop 0
	v_mfma_f32_16x16x32_bf16 v[12:15], v[144:147], v[176:179], v[12:15]
	v_mfma_f32_16x16x32_bf16 v[8:11], v[140:143], v[180:183], 0
	s_nop 0
	v_mfma_f32_16x16x32_bf16 v[8:11], v[136:139], v[176:179], v[8:11]
	v_mfma_f32_16x16x32_bf16 v[4:7], v[148:151], v[172:175], 0
	s_nop 0
	v_mfma_f32_16x16x32_bf16 v[4:7], v[144:147], v[168:171], v[4:7]
	v_mfma_f32_16x16x32_bf16 v[0:3], v[140:143], v[172:175], 0
	s_nop 0
	v_mfma_f32_16x16x32_bf16 v[0:3], v[136:139], v[168:171], v[0:3]
	s_setprio 0
	s_barrier
	ds_read_b128 v[164:167], v224
	ds_read_b128 v[160:163], v225
	ds_read_b128 v[156:159], v226
	ds_read_b128 v[152:155], v227
	ds_read_b128 v[148:151], v228
	ds_read_b128 v[144:147], v229
	ds_read_b128 v[140:143], v230
	ds_read_b128 v[136:139], v231
	ds_read_b128 v[168:171], v232 offset:32768
	ds_read_b128 v[172:175], v232 offset:33792
	ds_read_b128 v[176:179], v232 offset:34816
	ds_read_b128 v[180:183], v232 offset:35840
	ds_read_b128 v[184:187], v232 offset:36864
	ds_read_b128 v[188:191], v232 offset:37888
	ds_read_b128 v[192:195], v232 offset:38912
	ds_read_b128 v[196:199], v232 offset:39936
	s_mov_b32 m0, s68
	s_add_i32 s10, s60, 0x100100
	buffer_load_dwordx4 v213, s[12:15], s10 offen lds
	s_add_i32 s10, s60, 0x180100
	s_mov_b32 m0, s69
	s_nop 0
	buffer_load_dwordx4 v213, s[12:15], s10 offen lds
	s_waitcnt vmcnt(10)
	s_waitcnt lgkmcnt(8)
	s_barrier
	s_setprio 1
	s_waitcnt lgkmcnt(7)
	v_mfma_f32_16x16x32_bf16 v[124:127], v[164:167], v[168:171], v[124:127]
	s_waitcnt lgkmcnt(6)
	v_mfma_f32_16x16x32_bf16 v[124:127], v[160:163], v[172:175], v[124:127]
	v_mfma_f32_16x16x32_bf16 v[120:123], v[156:159], v[168:171], v[120:123]
	s_nop 0
	v_mfma_f32_16x16x32_bf16 v[120:123], v[152:155], v[172:175], v[120:123]
	s_waitcnt lgkmcnt(5)
	v_mfma_f32_16x16x32_bf16 v[116:119], v[164:167], v[176:179], v[116:119]
	s_waitcnt lgkmcnt(4)
	v_mfma_f32_16x16x32_bf16 v[116:119], v[160:163], v[180:183], v[116:119]
	v_mfma_f32_16x16x32_bf16 v[112:115], v[156:159], v[176:179], v[112:115]
	s_nop 0
	v_mfma_f32_16x16x32_bf16 v[112:115], v[152:155], v[180:183], v[112:115]
	s_waitcnt lgkmcnt(3)
	v_mfma_f32_16x16x32_bf16 v[108:111], v[164:167], v[184:187], v[108:111]
	s_waitcnt lgkmcnt(2)
	v_mfma_f32_16x16x32_bf16 v[108:111], v[160:163], v[188:191], v[108:111]
	v_mfma_f32_16x16x32_bf16 v[104:107], v[156:159], v[184:187], v[104:107]
	s_nop 0
	v_mfma_f32_16x16x32_bf16 v[104:107], v[152:155], v[188:191], v[104:107]
	s_waitcnt lgkmcnt(1)
	v_mfma_f32_16x16x32_bf16 v[100:103], v[164:167], v[192:195], v[100:103]
	s_waitcnt lgkmcnt(0)
	v_mfma_f32_16x16x32_bf16 v[100:103], v[160:163], v[196:199], v[100:103]
	v_mfma_f32_16x16x32_bf16 v[96:99], v[156:159], v[192:195], v[96:99]
	s_nop 0
	v_mfma_f32_16x16x32_bf16 v[96:99], v[152:155], v[196:199], v[96:99]
	s_setprio 0
	s_setprio 1
	v_mfma_f32_16x16x32_bf16 v[92:95], v[148:151], v[168:171], v[92:95]
	s_nop 0
	v_mfma_f32_16x16x32_bf16 v[92:95], v[144:147], v[172:175], v[92:95]
	v_mfma_f32_16x16x32_bf16 v[88:91], v[140:143], v[168:171], v[88:91]
	s_nop 0
	v_mfma_f32_16x16x32_bf16 v[88:91], v[136:139], v[172:175], v[88:91]
	v_mfma_f32_16x16x32_bf16 v[84:87], v[148:151], v[176:179], v[84:87]
	s_nop 0
	v_mfma_f32_16x16x32_bf16 v[84:87], v[144:147], v[180:183], v[84:87]
	v_mfma_f32_16x16x32_bf16 v[80:83], v[140:143], v[176:179], v[80:83]
	s_nop 0
	v_mfma_f32_16x16x32_bf16 v[80:83], v[136:139], v[180:183], v[80:83]
	v_mfma_f32_16x16x32_bf16 v[76:79], v[148:151], v[184:187], v[76:79]
	s_nop 0
	v_mfma_f32_16x16x32_bf16 v[76:79], v[144:147], v[188:191], v[76:79]
	v_mfma_f32_16x16x32_bf16 v[72:75], v[140:143], v[184:187], v[72:75]
	s_nop 0
	v_mfma_f32_16x16x32_bf16 v[72:75], v[136:139], v[188:191], v[72:75]
	v_mfma_f32_16x16x32_bf16 v[68:71], v[148:151], v[192:195], v[68:71]
	s_nop 0
	v_mfma_f32_16x16x32_bf16 v[68:71], v[144:147], v[196:199], v[68:71]
	v_mfma_f32_16x16x32_bf16 v[64:67], v[140:143], v[192:195], v[64:67]
	s_nop 0
	v_mfma_f32_16x16x32_bf16 v[64:67], v[136:139], v[196:199], v[64:67]
	s_setprio 0
	s_barrier
	ds_read_b128 v[168:171], v232 offset:49152
	ds_read_b128 v[172:175], v232 offset:50176
	ds_read_b128 v[176:179], v232 offset:51200
	ds_read_b128 v[180:183], v232 offset:52224
	ds_read_b128 v[184:187], v232 offset:53248
	ds_read_b128 v[188:191], v232 offset:54272
	ds_read_b128 v[192:195], v232 offset:55296
	ds_read_b128 v[196:199], v232 offset:56320
	s_mov_b32 m0, s72
	s_mov_b32 s10, s14
	s_mov_b32 s11, s15
	buffer_load_dwordx4 v214, s[8:11], s5 offen lds
	s_add_i32 s5, s42, 0x40180
	s_mov_b32 m0, s73
	s_nop 0
	buffer_load_dwordx4 v214, s[8:11], s5 offen lds
	s_add_i32 s5, s42, 0x4180
	s_mov_b32 m0, s76
	s_nop 0
	buffer_load_dwordx4 v214, s[8:11], s5 offen lds
	s_add_i32 s5, s42, 0x44180
	s_mov_b32 m0, s77
	s_nop 0
	buffer_load_dwordx4 v214, s[8:11], s5 offen lds
	s_mov_b32 m0, s74
	s_nop 0
	buffer_load_dwordx4 v213, s[12:15], s4 offen lds
	s_add_i32 s4, s60, 0x80180
	s_mov_b32 m0, s75
	s_nop 0
	buffer_load_dwordx4 v213, s[12:15], s4 offen lds
	s_waitcnt vmcnt(8)
	s_waitcnt lgkmcnt(6)
	s_barrier
	s_setprio 1
	v_mfma_f32_16x16x32_bf16 v[60:63], v[164:167], v[168:171], v[60:63]
	v_mfma_f32_16x16x32_bf16 v[60:63], v[160:163], v[172:175], v[60:63]
	v_mfma_f32_16x16x32_bf16 v[56:59], v[156:159], v[168:171], v[56:59]
	s_nop 0
	v_mfma_f32_16x16x32_bf16 v[56:59], v[152:155], v[172:175], v[56:59]
	s_waitcnt lgkmcnt(5)
	v_mfma_f32_16x16x32_bf16 v[52:55], v[164:167], v[176:179], v[52:55]
	s_waitcnt lgkmcnt(4)
	v_mfma_f32_16x16x32_bf16 v[52:55], v[160:163], v[180:183], v[52:55]
	v_mfma_f32_16x16x32_bf16 v[48:51], v[156:159], v[176:179], v[48:51]
	s_nop 0
	v_mfma_f32_16x16x32_bf16 v[48:51], v[152:155], v[180:183], v[48:51]
	s_waitcnt lgkmcnt(3)
	v_mfma_f32_16x16x32_bf16 v[44:47], v[164:167], v[184:187], v[44:47]
	s_waitcnt lgkmcnt(2)
	v_mfma_f32_16x16x32_bf16 v[44:47], v[160:163], v[188:191], v[44:47]
	v_mfma_f32_16x16x32_bf16 v[40:43], v[156:159], v[184:187], v[40:43]
	s_nop 0
	v_mfma_f32_16x16x32_bf16 v[40:43], v[152:155], v[188:191], v[40:43]
	s_waitcnt lgkmcnt(1)
	v_mfma_f32_16x16x32_bf16 v[36:39], v[164:167], v[192:195], v[36:39]
	s_waitcnt lgkmcnt(0)
	v_mfma_f32_16x16x32_bf16 v[36:39], v[160:163], v[196:199], v[36:39]
	v_mfma_f32_16x16x32_bf16 v[32:35], v[156:159], v[192:195], v[32:35]
	s_nop 0
	v_mfma_f32_16x16x32_bf16 v[32:35], v[152:155], v[196:199], v[32:35]
	s_setprio 0
	s_setprio 1
	v_mfma_f32_16x16x32_bf16 v[28:31], v[148:151], v[168:171], v[28:31]
	s_nop 0
	v_mfma_f32_16x16x32_bf16 v[28:31], v[144:147], v[172:175], v[28:31]
	v_mfma_f32_16x16x32_bf16 v[24:27], v[140:143], v[168:171], v[24:27]
	s_nop 0
	v_mfma_f32_16x16x32_bf16 v[24:27], v[136:139], v[172:175], v[24:27]
	v_mfma_f32_16x16x32_bf16 v[20:23], v[148:151], v[176:179], v[20:23]
	s_nop 0
	v_mfma_f32_16x16x32_bf16 v[20:23], v[144:147], v[180:183], v[20:23]
	v_mfma_f32_16x16x32_bf16 v[16:19], v[140:143], v[176:179], v[16:19]
	s_nop 0
	v_mfma_f32_16x16x32_bf16 v[16:19], v[136:139], v[180:183], v[16:19]
	v_mfma_f32_16x16x32_bf16 v[12:15], v[148:151], v[184:187], v[12:15]
	s_nop 0
	v_mfma_f32_16x16x32_bf16 v[12:15], v[144:147], v[188:191], v[12:15]
	v_mfma_f32_16x16x32_bf16 v[8:11], v[140:143], v[184:187], v[8:11]
	s_nop 0
	v_mfma_f32_16x16x32_bf16 v[8:11], v[136:139], v[188:191], v[8:11]
	v_mfma_f32_16x16x32_bf16 v[4:7], v[148:151], v[192:195], v[4:7]
	s_nop 0
	v_mfma_f32_16x16x32_bf16 v[4:7], v[144:147], v[196:199], v[4:7]
	v_mfma_f32_16x16x32_bf16 v[0:3], v[140:143], v[192:195], v[0:3]
	s_nop 0
	v_mfma_f32_16x16x32_bf16 v[0:3], v[136:139], v[196:199], v[0:3]
	s_setprio 0
	s_barrier
	s_waitcnt vmcnt(14)
	v_mul_f32_e32 v132, 0x42800000, v132
	v_mul_f32_e32 v128, 0x42800000, v128
	v_mul_f32_e32 v133, 0x42800000, v133
	v_mul_f32_e32 v129, 0x42800000, v129
	v_mul_f32_e32 v134, 0x42800000, v134
	v_mul_f32_e32 v130, 0x42800000, v130
	v_mul_f32_e32 v135, 0x42800000, v135
	v_mul_f32_e32 v131, 0x42800000, v131
	v_cvt_pk_fp8_f32 v202, v128, v132
	v_cvt_pk_fp8_f32 v233, v129, v133
	v_cvt_pk_fp8_f32 v234, v130, v134
	v_cvt_pk_fp8_f32 v235, v131, v135
	s_add_i32 s33, s42, 0x200
	s_mov_b32 s66, 0
	s_mov_b32 s89, s70
	s_mov_b32 s90, s71
	s_branch .LBB0_595

.LBB0_595:
	v_mov_b32_e32 v152, v202
	v_mov_b32_e32 v153, v233
	v_mov_b32_e32 v154, v234
	v_mov_b32_e32 v155, v235
	ds_read_b128 v[158:161], v216
	ds_read_b128 v[162:165], v217
	ds_read_b128 v[166:169], v218
	ds_read_b128 v[170:173], v219
	ds_read_b128 v[148:151], v220
	ds_read_b128 v[144:147], v221
	ds_read_b128 v[140:143], v222
	ds_read_b128 v[136:139], v223
	ds_read_b128 v[174:177], v232
	ds_read_b128 v[178:181], v232 offset:1024
	ds_read_b128 v[182:185], v232 offset:2048
	ds_read_b128 v[186:189], v232 offset:3072
	ds_read_b128 v[190:193], v232 offset:4096
	ds_read_b128 v[194:197], v232 offset:5120
	ds_read_b128 v[234:237], v232 offset:6144
	ds_read_b128 v[238:241], v232 offset:7168
	s_add_i32 s4, s60, s66
	s_mov_b32 s42, s90
	s_add_i32 s90, s90, 1
	s_add_i32 s5, s4, 0x200
	s_add_i32 s67, s33, s66
	s_cmpk_eq_i32 s66, 0x200
	s_cselect_b32 s43, s87, s5
	s_cselect_b32 s93, s88, s67
	s_add_i32 s92, s43, 0x80
	s_mov_b32 m0, s78
	s_add_i32 s5, s4, 0x100180
	buffer_load_dwordx4 v213, s[12:15], s5 offen lds
	s_add_i32 s4, s4, 0x180180
	s_mov_b32 m0, s81
	s_add_i32 s94, s93, 0x80
	buffer_load_dwordx4 v213, s[12:15], s4 offen lds
	s_lshr_b32 s4, s90, 2
	s_mul_i32 s67, s4, s34
	s_add_i32 s67, s67, s2
	s_cmp_lt_i32 s4, s3
	s_cselect_b64 s[4:5], -1, 0
	s_and_b64 s[96:97], s[4:5], exec
	s_cselect_b32 s91, s67, 0
	s_ashr_i32 s96, s91, 7
	s_bfe_u32 s95, s90, 0x10001
	s_ashr_i32 s97, s96, 31
	s_or_b32 s95, s95, s79
	s_lshl_b64 s[96:97], s[96:97], 23
	s_add_u32 s96, s48, s96
	s_addc_u32 s97, s49, s97
	s_lshl_b32 vcc_lo, s91, 16
	s_and_b32 vcc_lo, vcc_lo, 0x600000
	s_add_u32 s96, s96, vcc_lo
	s_addc_u32 s97, s97, 0
	s_lshl_b32 s91, s91, 7
	s_and_b32 s91, s91, 0xf80
	s_lshl_b32 vcc_lo, s91, 2
	s_add_u32 s96, s96, vcc_lo
	v_and_or_b32 v202, s89, 2, v200
	s_addc_u32 s97, s97, 0
	v_lshl_or_b32 v156, s95, 5, v215
	v_lshlrev_b64 v[128:129], 14, v[202:203]
	v_lshl_add_u64 v[128:129], s[96:97], 0, v[128:129]
	v_lshlrev_b32_e32 v202, 2, v156
	v_lshl_add_u64 v[128:129], v[128:129], 0, v[202:203]
	s_movk_i32 s95, 0x4000
	v_add_co_u32_e32 v132, vcc, s95, v128
	s_nop 1
	v_addc_co_u32_e32 v133, vcc, 0, v129, vcc
	global_load_dwordx4 v[128:131], v[128:129], off nt
	s_nop 0
	global_load_dwordx4 v[132:135], v[132:133], off nt
	s_waitcnt vmcnt(10)
	s_waitcnt lgkmcnt(8)
	s_barrier
	s_setprio 1
	s_waitcnt lgkmcnt(7)
	v_mfma_f32_16x16x32_bf16 v[124:127], v[158:161], v[174:177], v[124:127]
	s_waitcnt lgkmcnt(6)
	v_mfma_f32_16x16x32_bf16 v[124:127], v[162:165], v[178:181], v[124:127]
	v_mfma_f32_16x16x32_bf16 v[120:123], v[166:169], v[174:177], v[120:123]
	s_nop 0
	v_mfma_f32_16x16x32_bf16 v[120:123], v[170:173], v[178:181], v[120:123]
	s_waitcnt lgkmcnt(5)
	v_mfma_f32_16x16x32_bf16 v[116:119], v[158:161], v[182:185], v[116:119]
	s_waitcnt lgkmcnt(4)
	v_mfma_f32_16x16x32_bf16 v[116:119], v[162:165], v[186:189], v[116:119]
	v_mfma_f32_16x16x32_bf16 v[112:115], v[166:169], v[182:185], v[112:115]
	s_nop 0
	v_mfma_f32_16x16x32_bf16 v[112:115], v[170:173], v[186:189], v[112:115]
	s_waitcnt lgkmcnt(3)
	v_mfma_f32_16x16x32_bf16 v[108:111], v[158:161], v[190:193], v[108:111]
	s_waitcnt lgkmcnt(2)
	v_mfma_f32_16x16x32_bf16 v[108:111], v[162:165], v[194:197], v[108:111]
	v_mfma_f32_16x16x32_bf16 v[104:107], v[166:169], v[190:193], v[104:107]
	s_nop 0
	v_mfma_f32_16x16x32_bf16 v[104:107], v[170:173], v[194:197], v[104:107]
	s_waitcnt lgkmcnt(1)
	v_mfma_f32_16x16x32_bf16 v[100:103], v[158:161], v[234:237], v[100:103]
	s_waitcnt lgkmcnt(0)
	v_mfma_f32_16x16x32_bf16 v[100:103], v[162:165], v[238:241], v[100:103]
	v_mfma_f32_16x16x32_bf16 v[96:99], v[166:169], v[234:237], v[96:99]
	s_nop 0
	v_mfma_f32_16x16x32_bf16 v[96:99], v[170:173], v[238:241], v[96:99]
	s_setprio 0
	s_setprio 1
	v_mfma_f32_16x16x32_bf16 v[92:95], v[148:151], v[174:177], v[92:95]
	s_nop 0
	v_mfma_f32_16x16x32_bf16 v[92:95], v[144:147], v[178:181], v[92:95]
	v_mfma_f32_16x16x32_bf16 v[88:91], v[140:143], v[174:177], v[88:91]
	s_nop 0
	v_mfma_f32_16x16x32_bf16 v[88:91], v[136:139], v[178:181], v[88:91]
	v_mfma_f32_16x16x32_bf16 v[84:87], v[148:151], v[182:185], v[84:87]
	s_nop 0
	v_mfma_f32_16x16x32_bf16 v[84:87], v[144:147], v[186:189], v[84:87]
	v_mfma_f32_16x16x32_bf16 v[80:83], v[140:143], v[182:185], v[80:83]
	s_nop 0
	v_mfma_f32_16x16x32_bf16 v[80:83], v[136:139], v[186:189], v[80:83]
	v_mfma_f32_16x16x32_bf16 v[76:79], v[148:151], v[190:193], v[76:79]
	s_nop 0
	v_mfma_f32_16x16x32_bf16 v[76:79], v[144:147], v[194:197], v[76:79]
	v_mfma_f32_16x16x32_bf16 v[72:75], v[140:143], v[190:193], v[72:75]
	s_nop 0
	v_mfma_f32_16x16x32_bf16 v[72:75], v[136:139], v[194:197], v[72:75]
	v_mfma_f32_16x16x32_bf16 v[68:71], v[148:151], v[234:237], v[68:71]
	s_nop 0
	v_mfma_f32_16x16x32_bf16 v[68:71], v[144:147], v[238:241], v[68:71]
	v_mfma_f32_16x16x32_bf16 v[64:67], v[140:143], v[234:237], v[64:67]
	s_nop 0
	v_mfma_f32_16x16x32_bf16 v[64:67], v[136:139], v[238:241], v[64:67]
	s_setprio 0
	s_barrier
	ds_read_b128 v[174:177], v232 offset:16384
	ds_read_b128 v[178:181], v232 offset:17408
	ds_read_b128 v[182:185], v232 offset:18432
	ds_read_b128 v[186:189], v232 offset:19456
	ds_read_b128 v[190:193], v232 offset:20480
	ds_read_b128 v[194:197], v232 offset:21504
	ds_read_b128 v[234:237], v232 offset:22528
	ds_read_b128 v[238:241], v232 offset:23552
	s_mov_b32 m0, s47
	s_add_i32 s95, s93, 0x40000
	buffer_load_dwordx4 v214, s[8:11], s93 offen lds
	s_mov_b32 m0, s62
	s_nop 0
	buffer_load_dwordx4 v214, s[8:11], s95 offen lds
	s_add_i32 s95, s93, 0x4000
	s_mov_b32 m0, s63
	s_nop 0
	buffer_load_dwordx4 v214, s[8:11], s95 offen lds
	s_add_i32 s95, s93, 0x44000
	s_mov_b32 m0, s64
	s_nop 0
	buffer_load_dwordx4 v214, s[8:11], s95 offen lds
	s_mov_b32 m0, s46
	s_add_i32 s95, s43, 0x80000
	buffer_load_dwordx4 v213, s[12:15], s43 offen lds
	s_mov_b32 m0, s65
	s_nop 0
	buffer_load_dwordx4 v213, s[12:15], s95 offen lds
	s_waitcnt vmcnt(10)
	s_waitcnt lgkmcnt(6)
	s_barrier
	s_setprio 1
	v_mfma_f32_16x16x32_bf16 v[60:63], v[158:161], v[174:177], v[60:63]
	v_mfma_f32_16x16x32_bf16 v[60:63], v[162:165], v[178:181], v[60:63]
	v_mfma_f32_16x16x32_bf16 v[56:59], v[166:169], v[174:177], v[56:59]
	s_nop 0
	v_mfma_f32_16x16x32_bf16 v[56:59], v[170:173], v[178:181], v[56:59]
	s_waitcnt lgkmcnt(5)
	v_mfma_f32_16x16x32_bf16 v[52:55], v[158:161], v[182:185], v[52:55]
	s_waitcnt lgkmcnt(4)
	v_mfma_f32_16x16x32_bf16 v[52:55], v[162:165], v[186:189], v[52:55]
	v_mfma_f32_16x16x32_bf16 v[48:51], v[166:169], v[182:185], v[48:51]
	s_nop 0
	v_mfma_f32_16x16x32_bf16 v[48:51], v[170:173], v[186:189], v[48:51]
	s_waitcnt lgkmcnt(3)
	v_mfma_f32_16x16x32_bf16 v[44:47], v[158:161], v[190:193], v[44:47]
	s_waitcnt lgkmcnt(2)
	v_mfma_f32_16x16x32_bf16 v[44:47], v[162:165], v[194:197], v[44:47]
	v_mfma_f32_16x16x32_bf16 v[40:43], v[166:169], v[190:193], v[40:43]
	s_nop 0
	v_mfma_f32_16x16x32_bf16 v[40:43], v[170:173], v[194:197], v[40:43]
	s_waitcnt lgkmcnt(1)
	v_mfma_f32_16x16x32_bf16 v[36:39], v[158:161], v[234:237], v[36:39]
	s_waitcnt lgkmcnt(0)
	v_mfma_f32_16x16x32_bf16 v[36:39], v[162:165], v[238:241], v[36:39]
	v_mfma_f32_16x16x32_bf16 v[32:35], v[166:169], v[234:237], v[32:35]
	s_nop 0
	v_mfma_f32_16x16x32_bf16 v[32:35], v[170:173], v[238:241], v[32:35]
	s_setprio 0
	s_setprio 1
	v_mfma_f32_16x16x32_bf16 v[28:31], v[148:151], v[174:177], v[28:31]
	s_nop 0
	v_mfma_f32_16x16x32_bf16 v[28:31], v[144:147], v[178:181], v[28:31]
	v_mfma_f32_16x16x32_bf16 v[24:27], v[140:143], v[174:177], v[24:27]
	s_nop 0
	v_mfma_f32_16x16x32_bf16 v[24:27], v[136:139], v[178:181], v[24:27]
	v_mfma_f32_16x16x32_bf16 v[20:23], v[148:151], v[182:185], v[20:23]
	s_nop 0
	v_mfma_f32_16x16x32_bf16 v[20:23], v[144:147], v[186:189], v[20:23]
	v_mfma_f32_16x16x32_bf16 v[16:19], v[140:143], v[182:185], v[16:19]
	s_nop 0
	v_mfma_f32_16x16x32_bf16 v[16:19], v[136:139], v[186:189], v[16:19]
	v_mfma_f32_16x16x32_bf16 v[12:15], v[148:151], v[190:193], v[12:15]
	s_nop 0
	v_mfma_f32_16x16x32_bf16 v[12:15], v[144:147], v[194:197], v[12:15]
	v_mfma_f32_16x16x32_bf16 v[8:11], v[140:143], v[190:193], v[8:11]
	s_nop 0
	v_mfma_f32_16x16x32_bf16 v[8:11], v[136:139], v[194:197], v[8:11]
	v_mfma_f32_16x16x32_bf16 v[4:7], v[148:151], v[234:237], v[4:7]
	s_nop 0
	v_mfma_f32_16x16x32_bf16 v[4:7], v[144:147], v[238:241], v[4:7]
	v_mfma_f32_16x16x32_bf16 v[0:3], v[140:143], v[234:237], v[0:3]
	s_nop 0
	v_mfma_f32_16x16x32_bf16 v[0:3], v[136:139], v[238:241], v[0:3]
	s_setprio 0
	s_barrier
	ds_read_b128 v[136:139], v224
	ds_read_b128 v[140:143], v225
	ds_read_b128 v[144:147], v226
	ds_read_b128 v[148:151], v227
	ds_read_b128 v[158:161], v228
	ds_read_b128 v[162:165], v229
	ds_read_b128 v[166:169], v230
	ds_read_b128 v[170:173], v231
	ds_read_b128 v[174:177], v232 offset:32768
	ds_read_b128 v[178:181], v232 offset:33792
	ds_read_b128 v[182:185], v232 offset:34816
	ds_read_b128 v[186:189], v232 offset:35840
	ds_read_b128 v[190:193], v232 offset:36864
	ds_read_b128 v[194:197], v232 offset:37888
	ds_read_b128 v[234:237], v232 offset:38912
	ds_read_b128 v[238:241], v232 offset:39936
	s_mov_b32 m0, s68
	s_add_i32 s95, s43, 0x100000
	buffer_load_dwordx4 v213, s[12:15], s95 offen lds
	s_add_i32 s95, s43, 0x180000
	s_mov_b32 m0, s69
	s_nop 0
	buffer_load_dwordx4 v213, s[12:15], s95 offen lds
	s_waitcnt vmcnt(10)
	s_waitcnt lgkmcnt(8)
	s_barrier
	s_setprio 1
	s_waitcnt lgkmcnt(7)
	v_mfma_f32_16x16x32_bf16 v[124:127], v[136:139], v[174:177], v[124:127]
	s_waitcnt lgkmcnt(6)
	v_mfma_f32_16x16x32_bf16 v[124:127], v[140:143], v[178:181], v[124:127]
	v_mfma_f32_16x16x32_bf16 v[120:123], v[144:147], v[174:177], v[120:123]
	s_nop 0
	v_mfma_f32_16x16x32_bf16 v[120:123], v[148:151], v[178:181], v[120:123]
	s_waitcnt lgkmcnt(5)
	v_mfma_f32_16x16x32_bf16 v[116:119], v[136:139], v[182:185], v[116:119]
	s_waitcnt lgkmcnt(4)
	v_mfma_f32_16x16x32_bf16 v[116:119], v[140:143], v[186:189], v[116:119]
	v_mfma_f32_16x16x32_bf16 v[112:115], v[144:147], v[182:185], v[112:115]
	s_nop 0
	v_mfma_f32_16x16x32_bf16 v[112:115], v[148:151], v[186:189], v[112:115]
	s_waitcnt lgkmcnt(3)
	v_mfma_f32_16x16x32_bf16 v[108:111], v[136:139], v[190:193], v[108:111]
	s_waitcnt lgkmcnt(2)
	v_mfma_f32_16x16x32_bf16 v[108:111], v[140:143], v[194:197], v[108:111]
	v_mfma_f32_16x16x32_bf16 v[104:107], v[144:147], v[190:193], v[104:107]
	s_nop 0
	v_mfma_f32_16x16x32_bf16 v[104:107], v[148:151], v[194:197], v[104:107]
	s_waitcnt lgkmcnt(1)
	v_mfma_f32_16x16x32_bf16 v[100:103], v[136:139], v[234:237], v[100:103]
	s_waitcnt lgkmcnt(0)
	v_mfma_f32_16x16x32_bf16 v[100:103], v[140:143], v[238:241], v[100:103]
	v_mfma_f32_16x16x32_bf16 v[96:99], v[144:147], v[234:237], v[96:99]
	s_nop 0
	v_mfma_f32_16x16x32_bf16 v[96:99], v[148:151], v[238:241], v[96:99]
	s_setprio 0
	s_setprio 1
	v_mfma_f32_16x16x32_bf16 v[92:95], v[158:161], v[174:177], v[92:95]
	s_nop 0
	v_mfma_f32_16x16x32_bf16 v[92:95], v[162:165], v[178:181], v[92:95]
	v_mfma_f32_16x16x32_bf16 v[88:91], v[166:169], v[174:177], v[88:91]
	s_nop 0
	v_mfma_f32_16x16x32_bf16 v[88:91], v[170:173], v[178:181], v[88:91]
	v_mfma_f32_16x16x32_bf16 v[84:87], v[158:161], v[182:185], v[84:87]
	s_nop 0
	v_mfma_f32_16x16x32_bf16 v[84:87], v[162:165], v[186:189], v[84:87]
	v_mfma_f32_16x16x32_bf16 v[80:83], v[166:169], v[182:185], v[80:83]
	s_nop 0
	v_mfma_f32_16x16x32_bf16 v[80:83], v[170:173], v[186:189], v[80:83]
	v_mfma_f32_16x16x32_bf16 v[76:79], v[158:161], v[190:193], v[76:79]
	s_nop 0
	v_mfma_f32_16x16x32_bf16 v[76:79], v[162:165], v[194:197], v[76:79]
	v_mfma_f32_16x16x32_bf16 v[72:75], v[166:169], v[190:193], v[72:75]
	s_nop 0
	v_mfma_f32_16x16x32_bf16 v[72:75], v[170:173], v[194:197], v[72:75]
	v_mfma_f32_16x16x32_bf16 v[68:71], v[158:161], v[234:237], v[68:71]
	s_nop 0
	v_mfma_f32_16x16x32_bf16 v[68:71], v[162:165], v[238:241], v[68:71]
	v_mfma_f32_16x16x32_bf16 v[64:67], v[166:169], v[234:237], v[64:67]
	s_nop 0
	v_mfma_f32_16x16x32_bf16 v[64:67], v[170:173], v[238:241], v[64:67]
	s_setprio 0
	s_barrier
	ds_read_b128 v[174:177], v232 offset:49152
	ds_read_b128 v[178:181], v232 offset:50176
	ds_read_b128 v[182:185], v232 offset:51200
	ds_read_b128 v[186:189], v232 offset:52224
	ds_read_b128 v[190:193], v232 offset:53248
	ds_read_b128 v[194:197], v232 offset:54272
	ds_read_b128 v[234:237], v232 offset:55296
	ds_read_b128 v[238:241], v232 offset:56320
	s_mov_b32 m0, s72
	s_add_i32 s43, s43, 0x80080
	buffer_load_dwordx4 v214, s[8:11], s94 offen lds
	s_add_i32 s94, s93, 0x40080
	s_mov_b32 m0, s73
	s_nop 0
	buffer_load_dwordx4 v214, s[8:11], s94 offen lds
	s_add_i32 s94, s93, 0x4080
	s_mov_b32 m0, s76
	s_add_i32 s93, s93, 0x44080
	buffer_load_dwordx4 v214, s[8:11], s94 offen lds
	s_mov_b32 m0, s77
	s_nop 0
	buffer_load_dwordx4 v214, s[8:11], s93 offen lds
	s_mov_b32 m0, s74
	s_nop 0
	buffer_load_dwordx4 v213, s[12:15], s92 offen lds
	s_mov_b32 m0, s75
	s_nop 0
	buffer_load_dwordx4 v213, s[12:15], s43 offen lds
	s_waitcnt vmcnt(8)
	s_waitcnt lgkmcnt(6)
	s_barrier
	s_setprio 1
	v_mfma_f32_16x16x32_bf16 v[60:63], v[136:139], v[174:177], v[60:63]
	v_mfma_f32_16x16x32_bf16 v[60:63], v[140:143], v[178:181], v[60:63]
	v_mfma_f32_16x16x32_bf16 v[56:59], v[144:147], v[174:177], v[56:59]
	s_nop 0
	v_mfma_f32_16x16x32_bf16 v[56:59], v[148:151], v[178:181], v[56:59]
	s_waitcnt lgkmcnt(5)
	v_mfma_f32_16x16x32_bf16 v[52:55], v[136:139], v[182:185], v[52:55]
	s_waitcnt lgkmcnt(4)
	v_mfma_f32_16x16x32_bf16 v[52:55], v[140:143], v[186:189], v[52:55]
	v_mfma_f32_16x16x32_bf16 v[48:51], v[144:147], v[182:185], v[48:51]
	s_nop 0
	v_mfma_f32_16x16x32_bf16 v[48:51], v[148:151], v[186:189], v[48:51]
	s_waitcnt lgkmcnt(3)
	v_mfma_f32_16x16x32_bf16 v[44:47], v[136:139], v[190:193], v[44:47]
	s_waitcnt lgkmcnt(2)
	v_mfma_f32_16x16x32_bf16 v[44:47], v[140:143], v[194:197], v[44:47]
	v_mfma_f32_16x16x32_bf16 v[40:43], v[144:147], v[190:193], v[40:43]
	s_nop 0
	v_mfma_f32_16x16x32_bf16 v[40:43], v[148:151], v[194:197], v[40:43]
	s_waitcnt lgkmcnt(1)
	v_mfma_f32_16x16x32_bf16 v[36:39], v[136:139], v[234:237], v[36:39]
	s_waitcnt lgkmcnt(0)
	v_mfma_f32_16x16x32_bf16 v[36:39], v[140:143], v[238:241], v[36:39]
	v_mfma_f32_16x16x32_bf16 v[32:35], v[144:147], v[234:237], v[32:35]
	s_nop 0
	v_mfma_f32_16x16x32_bf16 v[32:35], v[148:151], v[238:241], v[32:35]
	s_setprio 0
	s_setprio 1
	v_mfma_f32_16x16x32_bf16 v[28:31], v[158:161], v[174:177], v[28:31]
	s_nop 0
	v_mfma_f32_16x16x32_bf16 v[28:31], v[162:165], v[178:181], v[28:31]
	v_mfma_f32_16x16x32_bf16 v[24:27], v[166:169], v[174:177], v[24:27]
	s_nop 0
	v_mfma_f32_16x16x32_bf16 v[24:27], v[170:173], v[178:181], v[24:27]
	v_mfma_f32_16x16x32_bf16 v[20:23], v[158:161], v[182:185], v[20:23]
	s_nop 0
	v_mfma_f32_16x16x32_bf16 v[20:23], v[162:165], v[186:189], v[20:23]
	v_mfma_f32_16x16x32_bf16 v[16:19], v[166:169], v[182:185], v[16:19]
	s_nop 0
	v_mfma_f32_16x16x32_bf16 v[16:19], v[170:173], v[186:189], v[16:19]
	v_mfma_f32_16x16x32_bf16 v[12:15], v[158:161], v[190:193], v[12:15]
	s_nop 0
	v_mfma_f32_16x16x32_bf16 v[12:15], v[162:165], v[194:197], v[12:15]
	v_mfma_f32_16x16x32_bf16 v[8:11], v[166:169], v[190:193], v[8:11]
	s_nop 0
	v_mfma_f32_16x16x32_bf16 v[8:11], v[170:173], v[194:197], v[8:11]
	v_mfma_f32_16x16x32_bf16 v[4:7], v[158:161], v[234:237], v[4:7]
	s_nop 0
	v_mfma_f32_16x16x32_bf16 v[4:7], v[162:165], v[238:241], v[4:7]
	v_mfma_f32_16x16x32_bf16 v[0:3], v[166:169], v[234:237], v[0:3]
	s_nop 0
	v_mfma_f32_16x16x32_bf16 v[0:3], v[170:173], v[238:241], v[0:3]
	s_setprio 0
	s_barrier
	s_bitcmp0_b32 s42, 0
	s_waitcnt vmcnt(15)
	v_mul_f32_e32 v128, 0x42800000, v128
	s_waitcnt vmcnt(14)
	v_mul_f32_e32 v132, 0x42800000, v132
	v_mul_f32_e32 v129, 0x42800000, v129
	v_mul_f32_e32 v133, 0x42800000, v133
	v_mul_f32_e32 v130, 0x42800000, v130
	v_mul_f32_e32 v134, 0x42800000, v134
	v_mul_f32_e32 v131, 0x42800000, v131
	v_mul_f32_e32 v135, 0x42800000, v135
	s_mov_b64 s[42:43], -1
	s_cbranch_scc0 .LBB0_598
	s_andn2_b64 vcc, exec, s[42:43]
	s_cbranch_vccnz .LBB0_594
	s_branch .LBB0_599
